# W2 plus: in every K-loop load segment all ds_read_b128 are issued first, scalar/vector address math and LDS-DMA issue after them
# speedup vs baseline: 1.0041x; 1.0041x over previous
.LBB0_310:
	s_ashr_i32 s91, s90, 31
	s_lshl_b64 s[4:5], s[90:91], 20
	s_add_u32 s62, s66, s4
	s_addc_u32 s63, s67, s5
	s_and_b64 s[4:5], s[36:37], exec
	s_cselect_b32 s4, s63, s25
	s_cselect_b32 s5, s62, s24
	s_ashr_i32 s89, s88, 31
	s_lshl_b64 s[20:21], s[88:89], 20
	s_add_u32 s20, s72, s20
	s_addc_u32 s21, s73, s21
	s_and_b64 s[30:31], s[36:37], exec
	s_cselect_b32 s8, s21, s1
	s_cselect_b32 s13, s20, s0
	s_add_u32 s17, s0, 0x10000
	s_addc_u32 s19, s1, 0
	s_add_u32 s0, s24, 0x80080
	s_addc_u32 s1, s25, 0
	s_mov_b32 s28, -2
	v_add_u32_e32 v100, s3, v190
	v_add_u32_e32 v156, s75, v190
	ds_read_b128 v[40:43], v100
	ds_read_b128 v[60:63], v100 offset:1024
	ds_read_b128 v[80:83], v100 offset:2048
	ds_read_b128 v[100:103], v100 offset:3072
	ds_read_b128 v[120:123], v156
	ds_read_b128 v[140:143], v156 offset:1024
	ds_read_b128 v[152:155], v156 offset:2048
	ds_read_b128 v[156:159], v156 offset:3072
	ds_read_b128 v[172:175], v191
	ds_read_b128 v[176:179], v191 offset:1024
	ds_read_b128 v[180:183], v191 offset:2048
	ds_read_b128 v[184:187], v191 offset:3072
	ds_read_b128 v[192:195], v191 offset:4096
	ds_read_b128 v[196:199], v191 offset:5120
	ds_read_b128 v[200:203], v191 offset:6144
	ds_read_b128 v[204:207], v191 offset:7168
	s_add_u32 s24, s0, 0xfff80080
	s_addc_u32 s25, s1, -1
	s_cmp_eq_u32 s28, 28
	s_cselect_b32 s39, s4, s25
	s_cselect_b32 s38, s5, s24
	s_cselect_b32 s25, s8, s19
	s_cselect_b32 s24, s13, s17
	v_lshl_add_u64 v[188:189], s[0:1], 0, v[168:169]
	s_add_i32 m0, s78, 0xc000
	s_nop 0
	global_load_lds_dwordx4 v[188:189], off
	v_lshl_add_u64 v[188:189], s[0:1], 0, v[170:171]
	s_add_i32 m0, s78, 0xe000
	s_nop 0
	global_load_lds_dwordx4 v[188:189], off
	s_waitcnt vmcnt(8)
	s_waitcnt lgkmcnt(0)
	s_setprio 1
	s_barrier
	v_mfma_f32_16x16x32_bf16 v[148:151], v[40:43], v[172:175], 0
	v_mfma_f32_16x16x32_bf16 v[144:147], v[80:83], v[172:175], 0
	v_mfma_f32_16x16x32_bf16 v[128:131], v[40:43], v[180:183], 0
	v_mfma_f32_16x16x32_bf16 v[124:127], v[80:83], v[180:183], 0
	v_mfma_f32_16x16x32_bf16 v[108:111], v[40:43], v[192:195], 0
	v_mfma_f32_16x16x32_bf16 v[104:107], v[80:83], v[192:195], 0
	v_mfma_f32_16x16x32_bf16 v[88:91], v[40:43], v[200:203], 0
	v_mfma_f32_16x16x32_bf16 v[84:87], v[80:83], v[200:203], 0
	v_mfma_f32_16x16x32_bf16 v[148:151], v[60:63], v[176:179], v[148:151]
	v_mfma_f32_16x16x32_bf16 v[144:147], v[100:103], v[176:179], v[144:147]
	v_mfma_f32_16x16x32_bf16 v[128:131], v[60:63], v[184:187], v[128:131]
	v_mfma_f32_16x16x32_bf16 v[124:127], v[100:103], v[184:187], v[124:127]
	v_mfma_f32_16x16x32_bf16 v[108:111], v[60:63], v[196:199], v[108:111]
	v_mfma_f32_16x16x32_bf16 v[104:107], v[100:103], v[196:199], v[104:107]
	v_mfma_f32_16x16x32_bf16 v[88:91], v[60:63], v[204:207], v[88:91]
	v_mfma_f32_16x16x32_bf16 v[84:87], v[100:103], v[204:207], v[84:87]
	s_setprio 0
	s_setprio 1
	v_mfma_f32_16x16x32_bf16 v[136:139], v[120:123], v[172:175], 0
	v_mfma_f32_16x16x32_bf16 v[132:135], v[152:155], v[172:175], 0
	v_mfma_f32_16x16x32_bf16 v[116:119], v[120:123], v[180:183], 0
	v_mfma_f32_16x16x32_bf16 v[112:115], v[152:155], v[180:183], 0
	v_mfma_f32_16x16x32_bf16 v[96:99], v[120:123], v[192:195], 0
	v_mfma_f32_16x16x32_bf16 v[92:95], v[152:155], v[192:195], 0
	v_mfma_f32_16x16x32_bf16 v[76:79], v[120:123], v[200:203], 0
	v_mfma_f32_16x16x32_bf16 v[72:75], v[152:155], v[200:203], 0
	v_mfma_f32_16x16x32_bf16 v[136:139], v[140:143], v[176:179], v[136:139]
	v_mfma_f32_16x16x32_bf16 v[132:135], v[156:159], v[176:179], v[132:135]
	v_mfma_f32_16x16x32_bf16 v[116:119], v[140:143], v[184:187], v[116:119]
	v_mfma_f32_16x16x32_bf16 v[112:115], v[156:159], v[184:187], v[112:115]
	v_mfma_f32_16x16x32_bf16 v[96:99], v[140:143], v[196:199], v[96:99]
	v_mfma_f32_16x16x32_bf16 v[92:95], v[156:159], v[196:199], v[92:95]
	v_mfma_f32_16x16x32_bf16 v[76:79], v[140:143], v[204:207], v[76:79]
	v_mfma_f32_16x16x32_bf16 v[72:75], v[156:159], v[204:207], v[72:75]
	s_barrier
	s_setprio 0
	ds_read_b128 v[172:175], v191 offset:16384
	ds_read_b128 v[176:179], v191 offset:17408
	ds_read_b128 v[180:183], v191 offset:18432
	ds_read_b128 v[184:187], v191 offset:19456
	ds_read_b128 v[192:195], v191 offset:20480
	ds_read_b128 v[196:199], v191 offset:21504
	ds_read_b128 v[200:203], v191 offset:22528
	ds_read_b128 v[204:207], v191 offset:23552
	s_mov_b32 m0, s23
	v_lshl_add_u64 v[188:189], s[24:25], 0, v[162:163]
	s_add_u32 s30, s24, 0x4000
	global_load_lds_dwordx4 v[188:189], off
	v_lshl_add_u64 v[188:189], s[24:25], 0, v[166:167]
	s_mov_b32 m0, s74
	s_addc_u32 s31, s25, 0
	global_load_lds_dwordx4 v[188:189], off
	v_lshl_add_u64 v[188:189], s[30:31], 0, v[162:163]
	s_mov_b32 m0, s76
	v_lshl_add_u64 v[208:209], s[38:39], 0, v[164:165]
	global_load_lds_dwordx4 v[188:189], off
	v_lshl_add_u64 v[188:189], s[30:31], 0, v[166:167]
	s_mov_b32 m0, s77
	s_nop 0
	global_load_lds_dwordx4 v[188:189], off
	v_lshl_add_u64 v[188:189], s[38:39], 0, v[160:161]
	s_mov_b32 m0, s78
	s_nop 0
	global_load_lds_dwordx4 v[188:189], off
	s_mov_b32 m0, s79
	s_nop 0
	global_load_lds_dwordx4 v[208:209], off
	s_waitcnt vmcnt(8)
	s_waitcnt lgkmcnt(0)
	s_setprio 1
	s_barrier
	v_mfma_f32_16x16x32_bf16 v[68:71], v[40:43], v[172:175], 0
	v_mfma_f32_16x16x32_bf16 v[64:67], v[80:83], v[172:175], 0
	v_mfma_f32_16x16x32_bf16 v[48:51], v[40:43], v[180:183], 0
	v_mfma_f32_16x16x32_bf16 v[44:47], v[80:83], v[180:183], 0
	v_mfma_f32_16x16x32_bf16 v[28:31], v[40:43], v[192:195], 0
	v_mfma_f32_16x16x32_bf16 v[24:27], v[80:83], v[192:195], 0
	v_mfma_f32_16x16x32_bf16 v[12:15], v[40:43], v[200:203], 0
	v_mfma_f32_16x16x32_bf16 v[8:11], v[80:83], v[200:203], 0
	v_mfma_f32_16x16x32_bf16 v[68:71], v[60:63], v[176:179], v[68:71]
	v_mfma_f32_16x16x32_bf16 v[64:67], v[100:103], v[176:179], v[64:67]
	v_mfma_f32_16x16x32_bf16 v[48:51], v[60:63], v[184:187], v[48:51]
	v_mfma_f32_16x16x32_bf16 v[44:47], v[100:103], v[184:187], v[44:47]
	v_mfma_f32_16x16x32_bf16 v[28:31], v[60:63], v[196:199], v[28:31]
	v_mfma_f32_16x16x32_bf16 v[24:27], v[100:103], v[196:199], v[24:27]
	v_mfma_f32_16x16x32_bf16 v[12:15], v[60:63], v[204:207], v[12:15]
	v_mfma_f32_16x16x32_bf16 v[8:11], v[100:103], v[204:207], v[8:11]
	s_setprio 0
	s_setprio 1
	v_mfma_f32_16x16x32_bf16 v[52:55], v[152:155], v[172:175], 0
	v_mfma_f32_16x16x32_bf16 v[36:39], v[120:123], v[180:183], 0
	v_mfma_f32_16x16x32_bf16 v[32:35], v[152:155], v[180:183], 0
	v_mfma_f32_16x16x32_bf16 v[20:23], v[120:123], v[192:195], 0
	v_mfma_f32_16x16x32_bf16 v[16:19], v[152:155], v[192:195], 0
	v_mfma_f32_16x16x32_bf16 v[4:7], v[120:123], v[200:203], 0
	v_mfma_f32_16x16x32_bf16 v[0:3], v[152:155], v[200:203], 0
	v_mfma_f32_16x16x32_bf16 v[40:43], v[120:123], v[172:175], 0
	v_mfma_f32_16x16x32_bf16 v[52:55], v[156:159], v[176:179], v[52:55]
	v_mfma_f32_16x16x32_bf16 v[36:39], v[140:143], v[184:187], v[36:39]
	v_mfma_f32_16x16x32_bf16 v[32:35], v[156:159], v[184:187], v[32:35]
	v_mfma_f32_16x16x32_bf16 v[20:23], v[140:143], v[196:199], v[20:23]
	v_mfma_f32_16x16x32_bf16 v[16:19], v[156:159], v[196:199], v[16:19]
	v_mfma_f32_16x16x32_bf16 v[4:7], v[140:143], v[204:207], v[4:7]
	v_mfma_f32_16x16x32_bf16 v[0:3], v[156:159], v[204:207], v[0:3]
	v_mfma_f32_16x16x32_bf16 v[40:43], v[140:143], v[176:179], v[40:43]
	s_barrier
	s_setprio 0
	v_add_u32_e32 v100, s86, v190
	v_add_u32_e32 v156, s95, v190
	ds_read_b128 v[56:59], v100
	ds_read_b128 v[60:63], v100 offset:1024
	ds_read_b128 v[80:83], v100 offset:2048
	ds_read_b128 v[100:103], v100 offset:3072
	ds_read_b128 v[120:123], v156
	ds_read_b128 v[140:143], v156 offset:1024
	ds_read_b128 v[152:155], v156 offset:2048
	ds_read_b128 v[156:159], v156 offset:3072
	ds_read_b128 v[172:175], v191 offset:32768
	ds_read_b128 v[176:179], v191 offset:33792
	ds_read_b128 v[180:183], v191 offset:34816
	ds_read_b128 v[184:187], v191 offset:35840
	ds_read_b128 v[192:195], v191 offset:36864
	ds_read_b128 v[196:199], v191 offset:37888
	ds_read_b128 v[200:203], v191 offset:38912
	ds_read_b128 v[204:207], v191 offset:39936
	s_add_u32 s30, s38, 0x80000
	s_addc_u32 s31, s39, 0
	s_mov_b32 m0, s82
	v_lshl_add_u64 v[210:211], s[30:31], 0, v[160:161]
	global_load_lds_dwordx4 v[210:211], off
	v_lshl_add_u64 v[210:211], s[30:31], 0, v[164:165]
	s_mov_b32 m0, s83
	s_nop 0
	global_load_lds_dwordx4 v[210:211], off
	s_waitcnt vmcnt(8)
	s_waitcnt lgkmcnt(0)
	s_setprio 1
	s_barrier
	v_mfma_f32_16x16x32_bf16 v[148:151], v[56:59], v[172:175], v[148:151]
	v_mfma_f32_16x16x32_bf16 v[144:147], v[80:83], v[172:175], v[144:147]
	v_mfma_f32_16x16x32_bf16 v[128:131], v[56:59], v[180:183], v[128:131]
	v_mfma_f32_16x16x32_bf16 v[124:127], v[80:83], v[180:183], v[124:127]
	v_mfma_f32_16x16x32_bf16 v[108:111], v[56:59], v[192:195], v[108:111]
	v_mfma_f32_16x16x32_bf16 v[104:107], v[80:83], v[192:195], v[104:107]
	v_mfma_f32_16x16x32_bf16 v[88:91], v[56:59], v[200:203], v[88:91]
	v_mfma_f32_16x16x32_bf16 v[84:87], v[80:83], v[200:203], v[84:87]
	v_mfma_f32_16x16x32_bf16 v[148:151], v[60:63], v[176:179], v[148:151]
	v_mfma_f32_16x16x32_bf16 v[144:147], v[100:103], v[176:179], v[144:147]
	v_mfma_f32_16x16x32_bf16 v[128:131], v[60:63], v[184:187], v[128:131]
	v_mfma_f32_16x16x32_bf16 v[124:127], v[100:103], v[184:187], v[124:127]
	v_mfma_f32_16x16x32_bf16 v[108:111], v[60:63], v[196:199], v[108:111]
	v_mfma_f32_16x16x32_bf16 v[104:107], v[100:103], v[196:199], v[104:107]
	v_mfma_f32_16x16x32_bf16 v[88:91], v[60:63], v[204:207], v[88:91]
	v_mfma_f32_16x16x32_bf16 v[84:87], v[100:103], v[204:207], v[84:87]
	s_setprio 0
	s_setprio 1
	v_mfma_f32_16x16x32_bf16 v[136:139], v[120:123], v[172:175], v[136:139]
	v_mfma_f32_16x16x32_bf16 v[132:135], v[152:155], v[172:175], v[132:135]
	v_mfma_f32_16x16x32_bf16 v[116:119], v[120:123], v[180:183], v[116:119]
	v_mfma_f32_16x16x32_bf16 v[112:115], v[152:155], v[180:183], v[112:115]
	v_mfma_f32_16x16x32_bf16 v[96:99], v[120:123], v[192:195], v[96:99]
	v_mfma_f32_16x16x32_bf16 v[92:95], v[152:155], v[192:195], v[92:95]
	v_mfma_f32_16x16x32_bf16 v[76:79], v[120:123], v[200:203], v[76:79]
	v_mfma_f32_16x16x32_bf16 v[72:75], v[152:155], v[200:203], v[72:75]
	v_mfma_f32_16x16x32_bf16 v[136:139], v[140:143], v[176:179], v[136:139]
	v_mfma_f32_16x16x32_bf16 v[132:135], v[156:159], v[176:179], v[132:135]
	v_mfma_f32_16x16x32_bf16 v[116:119], v[140:143], v[184:187], v[116:119]
	v_mfma_f32_16x16x32_bf16 v[112:115], v[156:159], v[184:187], v[112:115]
	v_mfma_f32_16x16x32_bf16 v[96:99], v[140:143], v[196:199], v[96:99]
	v_mfma_f32_16x16x32_bf16 v[92:95], v[156:159], v[196:199], v[92:95]
	v_mfma_f32_16x16x32_bf16 v[76:79], v[140:143], v[204:207], v[76:79]
	v_mfma_f32_16x16x32_bf16 v[72:75], v[156:159], v[204:207], v[72:75]
	s_barrier
	s_setprio 0
	ds_read_b128 v[172:175], v191 offset:49152
	ds_read_b128 v[176:179], v191 offset:50176
	ds_read_b128 v[180:183], v191 offset:51200
	ds_read_b128 v[184:187], v191 offset:52224
	ds_read_b128 v[192:195], v191 offset:53248
	ds_read_b128 v[196:199], v191 offset:54272
	ds_read_b128 v[200:203], v191 offset:55296
	ds_read_b128 v[204:207], v191 offset:56320
	s_add_u32 s30, s24, 0x8000
	s_addc_u32 s31, s25, 0
	s_mov_b32 m0, s87
	v_lshl_add_u64 v[210:211], s[30:31], 0, v[162:163]
	s_add_u32 s24, s24, 0xc000
	global_load_lds_dwordx4 v[210:211], off
	v_lshl_add_u64 v[210:211], s[30:31], 0, v[166:167]
	s_mov_b32 m0, s92
	s_addc_u32 s25, s25, 0
	global_load_lds_dwordx4 v[210:211], off
	v_lshl_add_u64 v[210:211], s[24:25], 0, v[162:163]
	s_mov_b32 m0, s96
	v_lshl_add_u64 v[188:189], v[188:189], 0, s[26:27]
	global_load_lds_dwordx4 v[210:211], off
	v_lshl_add_u64 v[210:211], s[24:25], 0, v[166:167]
	s_mov_b32 m0, s97
	s_nop 0
	global_load_lds_dwordx4 v[210:211], off
	s_mov_b32 m0, s93
	s_nop 0
	global_load_lds_dwordx4 v[188:189], off
	v_lshl_add_u64 v[188:189], v[208:209], 0, s[26:27]
	s_mov_b32 m0, s94
	s_nop 0
	global_load_lds_dwordx4 v[188:189], off
	s_waitcnt vmcnt(8)
	s_waitcnt lgkmcnt(0)
	s_setprio 1
	s_barrier
	v_mfma_f32_16x16x32_bf16 v[68:71], v[56:59], v[172:175], v[68:71]
	v_mfma_f32_16x16x32_bf16 v[64:67], v[80:83], v[172:175], v[64:67]
	v_mfma_f32_16x16x32_bf16 v[48:51], v[56:59], v[180:183], v[48:51]
	v_mfma_f32_16x16x32_bf16 v[44:47], v[80:83], v[180:183], v[44:47]
	v_mfma_f32_16x16x32_bf16 v[28:31], v[56:59], v[192:195], v[28:31]
	v_mfma_f32_16x16x32_bf16 v[24:27], v[80:83], v[192:195], v[24:27]
	v_mfma_f32_16x16x32_bf16 v[12:15], v[56:59], v[200:203], v[12:15]
	v_mfma_f32_16x16x32_bf16 v[8:11], v[80:83], v[200:203], v[8:11]
	v_mfma_f32_16x16x32_bf16 v[68:71], v[60:63], v[176:179], v[68:71]
	v_mfma_f32_16x16x32_bf16 v[64:67], v[100:103], v[176:179], v[64:67]
	v_mfma_f32_16x16x32_bf16 v[48:51], v[60:63], v[184:187], v[48:51]
	v_mfma_f32_16x16x32_bf16 v[44:47], v[100:103], v[184:187], v[44:47]
	v_mfma_f32_16x16x32_bf16 v[28:31], v[60:63], v[196:199], v[28:31]
	v_mfma_f32_16x16x32_bf16 v[24:27], v[100:103], v[196:199], v[24:27]
	v_mfma_f32_16x16x32_bf16 v[12:15], v[60:63], v[204:207], v[12:15]
	v_mfma_f32_16x16x32_bf16 v[8:11], v[100:103], v[204:207], v[8:11]
	s_setprio 0
	s_setprio 1
	v_mfma_f32_16x16x32_bf16 v[40:43], v[120:123], v[172:175], v[40:43]
	v_mfma_f32_16x16x32_bf16 v[56:59], v[140:143], v[176:179], v[40:43]
	v_mfma_f32_16x16x32_bf16 v[40:43], v[152:155], v[172:175], v[52:55]
	v_mfma_f32_16x16x32_bf16 v[36:39], v[120:123], v[180:183], v[36:39]
	v_mfma_f32_16x16x32_bf16 v[32:35], v[152:155], v[180:183], v[32:35]
	v_mfma_f32_16x16x32_bf16 v[20:23], v[120:123], v[192:195], v[20:23]
	v_mfma_f32_16x16x32_bf16 v[16:19], v[152:155], v[192:195], v[16:19]
	v_mfma_f32_16x16x32_bf16 v[4:7], v[120:123], v[200:203], v[4:7]
	v_mfma_f32_16x16x32_bf16 v[0:3], v[152:155], v[200:203], v[0:3]
	v_mfma_f32_16x16x32_bf16 v[52:55], v[156:159], v[176:179], v[40:43]
	v_mfma_f32_16x16x32_bf16 v[36:39], v[140:143], v[184:187], v[36:39]
	v_mfma_f32_16x16x32_bf16 v[32:35], v[156:159], v[184:187], v[32:35]
	v_mfma_f32_16x16x32_bf16 v[20:23], v[140:143], v[196:199], v[20:23]
	v_mfma_f32_16x16x32_bf16 v[16:19], v[156:159], v[196:199], v[16:19]
	v_mfma_f32_16x16x32_bf16 v[4:7], v[140:143], v[204:207], v[4:7]
	v_mfma_f32_16x16x32_bf16 v[0:3], v[156:159], v[204:207], v[0:3]
	s_barrier
	s_setprio 0
	s_add_i32 s28, s28, 2
	s_add_u32 s17, s17, 0x10000
	s_addc_u32 s19, s19, 0
	s_add_u32 s0, s0, 0x100
	s_addc_u32 s1, s1, 0
	s_cmp_gt_u32 s28, 29
.LBB0_311:
	v_add_u32_e32 v100, s3, v190
	v_add_u32_e32 v156, s75, v190
	ds_read_b128 v[40:43], v100
	ds_read_b128 v[60:63], v100 offset:1024
	ds_read_b128 v[80:83], v100 offset:2048
	ds_read_b128 v[100:103], v100 offset:3072
	ds_read_b128 v[120:123], v156
	ds_read_b128 v[140:143], v156 offset:1024
	ds_read_b128 v[152:155], v156 offset:2048
	ds_read_b128 v[156:159], v156 offset:3072
	ds_read_b128 v[172:175], v191
	ds_read_b128 v[176:179], v191 offset:1024
	ds_read_b128 v[180:183], v191 offset:2048
	ds_read_b128 v[184:187], v191 offset:3072
	ds_read_b128 v[192:195], v191 offset:4096
	ds_read_b128 v[196:199], v191 offset:5120
	ds_read_b128 v[200:203], v191 offset:6144
	ds_read_b128 v[204:207], v191 offset:7168
	s_add_u32 s24, s0, 0xfff80080
	s_addc_u32 s25, s1, -1
	s_cmp_eq_u32 s28, 28
	s_cselect_b32 s39, s4, s25
	s_cselect_b32 s38, s5, s24
	s_cselect_b32 s25, s8, s19
	s_cselect_b32 s24, s13, s17
	v_lshl_add_u64 v[188:189], s[0:1], 0, v[168:169]
	s_add_i32 m0, s78, 0xc000
	s_nop 0
	global_load_lds_dwordx4 v[188:189], off
	v_lshl_add_u64 v[188:189], s[0:1], 0, v[170:171]
	s_add_i32 m0, s78, 0xe000
	s_nop 0
	global_load_lds_dwordx4 v[188:189], off
	s_waitcnt vmcnt(8)
	s_waitcnt lgkmcnt(0)
	s_setprio 1
	s_barrier
	v_mfma_f32_16x16x32_bf16 v[148:151], v[40:43], v[172:175], v[148:151]
	v_mfma_f32_16x16x32_bf16 v[144:147], v[80:83], v[172:175], v[144:147]
	v_mfma_f32_16x16x32_bf16 v[128:131], v[40:43], v[180:183], v[128:131]
	v_mfma_f32_16x16x32_bf16 v[124:127], v[80:83], v[180:183], v[124:127]
	v_mfma_f32_16x16x32_bf16 v[108:111], v[40:43], v[192:195], v[108:111]
	v_mfma_f32_16x16x32_bf16 v[104:107], v[80:83], v[192:195], v[104:107]
	v_mfma_f32_16x16x32_bf16 v[88:91], v[40:43], v[200:203], v[88:91]
	v_mfma_f32_16x16x32_bf16 v[84:87], v[80:83], v[200:203], v[84:87]
	v_mfma_f32_16x16x32_bf16 v[148:151], v[60:63], v[176:179], v[148:151]
	v_mfma_f32_16x16x32_bf16 v[144:147], v[100:103], v[176:179], v[144:147]
	v_mfma_f32_16x16x32_bf16 v[128:131], v[60:63], v[184:187], v[128:131]
	v_mfma_f32_16x16x32_bf16 v[124:127], v[100:103], v[184:187], v[124:127]
	v_mfma_f32_16x16x32_bf16 v[108:111], v[60:63], v[196:199], v[108:111]
	v_mfma_f32_16x16x32_bf16 v[104:107], v[100:103], v[196:199], v[104:107]
	v_mfma_f32_16x16x32_bf16 v[88:91], v[60:63], v[204:207], v[88:91]
	v_mfma_f32_16x16x32_bf16 v[84:87], v[100:103], v[204:207], v[84:87]
	s_setprio 0
	s_setprio 1
	v_mfma_f32_16x16x32_bf16 v[136:139], v[120:123], v[172:175], v[136:139]
	v_mfma_f32_16x16x32_bf16 v[132:135], v[152:155], v[172:175], v[132:135]
	v_mfma_f32_16x16x32_bf16 v[116:119], v[120:123], v[180:183], v[116:119]
	v_mfma_f32_16x16x32_bf16 v[112:115], v[152:155], v[180:183], v[112:115]
	v_mfma_f32_16x16x32_bf16 v[96:99], v[120:123], v[192:195], v[96:99]
	v_mfma_f32_16x16x32_bf16 v[92:95], v[152:155], v[192:195], v[92:95]
	v_mfma_f32_16x16x32_bf16 v[76:79], v[120:123], v[200:203], v[76:79]
	v_mfma_f32_16x16x32_bf16 v[72:75], v[152:155], v[200:203], v[72:75]
	v_mfma_f32_16x16x32_bf16 v[136:139], v[140:143], v[176:179], v[136:139]
	v_mfma_f32_16x16x32_bf16 v[132:135], v[156:159], v[176:179], v[132:135]
	v_mfma_f32_16x16x32_bf16 v[116:119], v[140:143], v[184:187], v[116:119]
	v_mfma_f32_16x16x32_bf16 v[112:115], v[156:159], v[184:187], v[112:115]
	v_mfma_f32_16x16x32_bf16 v[96:99], v[140:143], v[196:199], v[96:99]
	v_mfma_f32_16x16x32_bf16 v[92:95], v[156:159], v[196:199], v[92:95]
	v_mfma_f32_16x16x32_bf16 v[76:79], v[140:143], v[204:207], v[76:79]
	v_mfma_f32_16x16x32_bf16 v[72:75], v[156:159], v[204:207], v[72:75]
	s_barrier
	s_setprio 0
	ds_read_b128 v[172:175], v191 offset:16384
	ds_read_b128 v[176:179], v191 offset:17408
	ds_read_b128 v[180:183], v191 offset:18432
	ds_read_b128 v[184:187], v191 offset:19456
	ds_read_b128 v[192:195], v191 offset:20480
	ds_read_b128 v[196:199], v191 offset:21504
	ds_read_b128 v[200:203], v191 offset:22528
	ds_read_b128 v[204:207], v191 offset:23552
	s_mov_b32 m0, s23
	v_lshl_add_u64 v[188:189], s[24:25], 0, v[162:163]
	s_add_u32 s30, s24, 0x4000
	global_load_lds_dwordx4 v[188:189], off
	v_lshl_add_u64 v[188:189], s[24:25], 0, v[166:167]
	s_mov_b32 m0, s74
	s_addc_u32 s31, s25, 0
	global_load_lds_dwordx4 v[188:189], off
	v_lshl_add_u64 v[188:189], s[30:31], 0, v[162:163]
	s_mov_b32 m0, s76
	v_lshl_add_u64 v[208:209], s[38:39], 0, v[164:165]
	global_load_lds_dwordx4 v[188:189], off
	v_lshl_add_u64 v[188:189], s[30:31], 0, v[166:167]
	s_mov_b32 m0, s77
	s_nop 0
	global_load_lds_dwordx4 v[188:189], off
	v_lshl_add_u64 v[188:189], s[38:39], 0, v[160:161]
	s_mov_b32 m0, s78
	s_nop 0
	global_load_lds_dwordx4 v[188:189], off
	s_mov_b32 m0, s79
	s_nop 0
	global_load_lds_dwordx4 v[208:209], off
	s_waitcnt vmcnt(8)
	s_waitcnt lgkmcnt(0)
	s_setprio 1
	s_barrier
	v_mfma_f32_16x16x32_bf16 v[68:71], v[40:43], v[172:175], v[68:71]
	v_mfma_f32_16x16x32_bf16 v[64:67], v[80:83], v[172:175], v[64:67]
	v_mfma_f32_16x16x32_bf16 v[48:51], v[40:43], v[180:183], v[48:51]
	v_mfma_f32_16x16x32_bf16 v[44:47], v[80:83], v[180:183], v[44:47]
	v_mfma_f32_16x16x32_bf16 v[28:31], v[40:43], v[192:195], v[28:31]
	v_mfma_f32_16x16x32_bf16 v[24:27], v[80:83], v[192:195], v[24:27]
	v_mfma_f32_16x16x32_bf16 v[12:15], v[40:43], v[200:203], v[12:15]
	v_mfma_f32_16x16x32_bf16 v[8:11], v[80:83], v[200:203], v[8:11]
	v_mfma_f32_16x16x32_bf16 v[68:71], v[60:63], v[176:179], v[68:71]
	v_mfma_f32_16x16x32_bf16 v[64:67], v[100:103], v[176:179], v[64:67]
	v_mfma_f32_16x16x32_bf16 v[48:51], v[60:63], v[184:187], v[48:51]
	v_mfma_f32_16x16x32_bf16 v[44:47], v[100:103], v[184:187], v[44:47]
	v_mfma_f32_16x16x32_bf16 v[28:31], v[60:63], v[196:199], v[28:31]
	v_mfma_f32_16x16x32_bf16 v[24:27], v[100:103], v[196:199], v[24:27]
	v_mfma_f32_16x16x32_bf16 v[12:15], v[60:63], v[204:207], v[12:15]
	v_mfma_f32_16x16x32_bf16 v[8:11], v[100:103], v[204:207], v[8:11]
	s_setprio 0
	s_setprio 1
	v_mfma_f32_16x16x32_bf16 v[52:55], v[152:155], v[172:175], v[52:55]
	v_mfma_f32_16x16x32_bf16 v[36:39], v[120:123], v[180:183], v[36:39]
	v_mfma_f32_16x16x32_bf16 v[32:35], v[152:155], v[180:183], v[32:35]
	v_mfma_f32_16x16x32_bf16 v[20:23], v[120:123], v[192:195], v[20:23]
	v_mfma_f32_16x16x32_bf16 v[16:19], v[152:155], v[192:195], v[16:19]
	v_mfma_f32_16x16x32_bf16 v[4:7], v[120:123], v[200:203], v[4:7]
	v_mfma_f32_16x16x32_bf16 v[0:3], v[152:155], v[200:203], v[0:3]
	v_mfma_f32_16x16x32_bf16 v[40:43], v[120:123], v[172:175], v[56:59]
	v_mfma_f32_16x16x32_bf16 v[52:55], v[156:159], v[176:179], v[52:55]
	v_mfma_f32_16x16x32_bf16 v[36:39], v[140:143], v[184:187], v[36:39]
	v_mfma_f32_16x16x32_bf16 v[32:35], v[156:159], v[184:187], v[32:35]
	v_mfma_f32_16x16x32_bf16 v[20:23], v[140:143], v[196:199], v[20:23]
	v_mfma_f32_16x16x32_bf16 v[16:19], v[156:159], v[196:199], v[16:19]
	v_mfma_f32_16x16x32_bf16 v[4:7], v[140:143], v[204:207], v[4:7]
	v_mfma_f32_16x16x32_bf16 v[0:3], v[156:159], v[204:207], v[0:3]
	v_mfma_f32_16x16x32_bf16 v[40:43], v[140:143], v[176:179], v[40:43]
	s_barrier
	s_setprio 0
	v_add_u32_e32 v100, s86, v190
	v_add_u32_e32 v156, s95, v190
	ds_read_b128 v[56:59], v100
	ds_read_b128 v[60:63], v100 offset:1024
	ds_read_b128 v[80:83], v100 offset:2048
	ds_read_b128 v[100:103], v100 offset:3072
	ds_read_b128 v[120:123], v156
	ds_read_b128 v[140:143], v156 offset:1024
	ds_read_b128 v[152:155], v156 offset:2048
	ds_read_b128 v[156:159], v156 offset:3072
	ds_read_b128 v[172:175], v191 offset:32768
	ds_read_b128 v[176:179], v191 offset:33792
	ds_read_b128 v[180:183], v191 offset:34816
	ds_read_b128 v[184:187], v191 offset:35840
	ds_read_b128 v[192:195], v191 offset:36864
	ds_read_b128 v[196:199], v191 offset:37888
	ds_read_b128 v[200:203], v191 offset:38912
	ds_read_b128 v[204:207], v191 offset:39936
	s_add_u32 s30, s38, 0x80000
	s_addc_u32 s31, s39, 0
	s_mov_b32 m0, s82
	v_lshl_add_u64 v[210:211], s[30:31], 0, v[160:161]
	global_load_lds_dwordx4 v[210:211], off
	v_lshl_add_u64 v[210:211], s[30:31], 0, v[164:165]
	s_mov_b32 m0, s83
	s_nop 0
	global_load_lds_dwordx4 v[210:211], off
	s_waitcnt vmcnt(8)
	s_waitcnt lgkmcnt(0)
	s_setprio 1
	s_barrier
	v_mfma_f32_16x16x32_bf16 v[148:151], v[56:59], v[172:175], v[148:151]
	v_mfma_f32_16x16x32_bf16 v[144:147], v[80:83], v[172:175], v[144:147]
	v_mfma_f32_16x16x32_bf16 v[128:131], v[56:59], v[180:183], v[128:131]
	v_mfma_f32_16x16x32_bf16 v[124:127], v[80:83], v[180:183], v[124:127]
	v_mfma_f32_16x16x32_bf16 v[108:111], v[56:59], v[192:195], v[108:111]
	v_mfma_f32_16x16x32_bf16 v[104:107], v[80:83], v[192:195], v[104:107]
	v_mfma_f32_16x16x32_bf16 v[88:91], v[56:59], v[200:203], v[88:91]
	v_mfma_f32_16x16x32_bf16 v[84:87], v[80:83], v[200:203], v[84:87]
	v_mfma_f32_16x16x32_bf16 v[148:151], v[60:63], v[176:179], v[148:151]
	v_mfma_f32_16x16x32_bf16 v[144:147], v[100:103], v[176:179], v[144:147]
	v_mfma_f32_16x16x32_bf16 v[128:131], v[60:63], v[184:187], v[128:131]
	v_mfma_f32_16x16x32_bf16 v[124:127], v[100:103], v[184:187], v[124:127]
	v_mfma_f32_16x16x32_bf16 v[108:111], v[60:63], v[196:199], v[108:111]
	v_mfma_f32_16x16x32_bf16 v[104:107], v[100:103], v[196:199], v[104:107]
	v_mfma_f32_16x16x32_bf16 v[88:91], v[60:63], v[204:207], v[88:91]
	v_mfma_f32_16x16x32_bf16 v[84:87], v[100:103], v[204:207], v[84:87]
	s_setprio 0
	s_setprio 1
	v_mfma_f32_16x16x32_bf16 v[136:139], v[120:123], v[172:175], v[136:139]
	v_mfma_f32_16x16x32_bf16 v[132:135], v[152:155], v[172:175], v[132:135]
	v_mfma_f32_16x16x32_bf16 v[116:119], v[120:123], v[180:183], v[116:119]
	v_mfma_f32_16x16x32_bf16 v[112:115], v[152:155], v[180:183], v[112:115]
	v_mfma_f32_16x16x32_bf16 v[96:99], v[120:123], v[192:195], v[96:99]
	v_mfma_f32_16x16x32_bf16 v[92:95], v[152:155], v[192:195], v[92:95]
	v_mfma_f32_16x16x32_bf16 v[76:79], v[120:123], v[200:203], v[76:79]
	v_mfma_f32_16x16x32_bf16 v[72:75], v[152:155], v[200:203], v[72:75]
	v_mfma_f32_16x16x32_bf16 v[136:139], v[140:143], v[176:179], v[136:139]
	v_mfma_f32_16x16x32_bf16 v[132:135], v[156:159], v[176:179], v[132:135]
	v_mfma_f32_16x16x32_bf16 v[116:119], v[140:143], v[184:187], v[116:119]
	v_mfma_f32_16x16x32_bf16 v[112:115], v[156:159], v[184:187], v[112:115]
	v_mfma_f32_16x16x32_bf16 v[96:99], v[140:143], v[196:199], v[96:99]
	v_mfma_f32_16x16x32_bf16 v[92:95], v[156:159], v[196:199], v[92:95]
	v_mfma_f32_16x16x32_bf16 v[76:79], v[140:143], v[204:207], v[76:79]
	v_mfma_f32_16x16x32_bf16 v[72:75], v[156:159], v[204:207], v[72:75]
	s_barrier
	s_setprio 0
	ds_read_b128 v[172:175], v191 offset:49152
	ds_read_b128 v[176:179], v191 offset:50176
	ds_read_b128 v[180:183], v191 offset:51200
	ds_read_b128 v[184:187], v191 offset:52224
	ds_read_b128 v[192:195], v191 offset:53248
	ds_read_b128 v[196:199], v191 offset:54272
	ds_read_b128 v[200:203], v191 offset:55296
	ds_read_b128 v[204:207], v191 offset:56320
	s_add_u32 s30, s24, 0x8000
	s_addc_u32 s31, s25, 0
	s_mov_b32 m0, s87
	v_lshl_add_u64 v[210:211], s[30:31], 0, v[162:163]
	s_add_u32 s24, s24, 0xc000
	global_load_lds_dwordx4 v[210:211], off
	v_lshl_add_u64 v[210:211], s[30:31], 0, v[166:167]
	s_mov_b32 m0, s92
	s_addc_u32 s25, s25, 0
	global_load_lds_dwordx4 v[210:211], off
	v_lshl_add_u64 v[210:211], s[24:25], 0, v[162:163]
	s_mov_b32 m0, s96
	v_lshl_add_u64 v[188:189], v[188:189], 0, s[26:27]
	global_load_lds_dwordx4 v[210:211], off
	v_lshl_add_u64 v[210:211], s[24:25], 0, v[166:167]
	s_mov_b32 m0, s97
	s_nop 0
	global_load_lds_dwordx4 v[210:211], off
	s_mov_b32 m0, s93
	s_nop 0
	global_load_lds_dwordx4 v[188:189], off
	v_lshl_add_u64 v[188:189], v[208:209], 0, s[26:27]
	s_mov_b32 m0, s94
	s_nop 0
	global_load_lds_dwordx4 v[188:189], off
	s_waitcnt vmcnt(8)
	s_waitcnt lgkmcnt(0)
	s_setprio 1
	s_barrier
	v_mfma_f32_16x16x32_bf16 v[68:71], v[56:59], v[172:175], v[68:71]
	v_mfma_f32_16x16x32_bf16 v[64:67], v[80:83], v[172:175], v[64:67]
	v_mfma_f32_16x16x32_bf16 v[48:51], v[56:59], v[180:183], v[48:51]
	v_mfma_f32_16x16x32_bf16 v[44:47], v[80:83], v[180:183], v[44:47]
	v_mfma_f32_16x16x32_bf16 v[28:31], v[56:59], v[192:195], v[28:31]
	v_mfma_f32_16x16x32_bf16 v[24:27], v[80:83], v[192:195], v[24:27]
	v_mfma_f32_16x16x32_bf16 v[12:15], v[56:59], v[200:203], v[12:15]
	v_mfma_f32_16x16x32_bf16 v[8:11], v[80:83], v[200:203], v[8:11]
	v_mfma_f32_16x16x32_bf16 v[68:71], v[60:63], v[176:179], v[68:71]
	v_mfma_f32_16x16x32_bf16 v[64:67], v[100:103], v[176:179], v[64:67]
	v_mfma_f32_16x16x32_bf16 v[48:51], v[60:63], v[184:187], v[48:51]
	v_mfma_f32_16x16x32_bf16 v[44:47], v[100:103], v[184:187], v[44:47]
	v_mfma_f32_16x16x32_bf16 v[28:31], v[60:63], v[196:199], v[28:31]
	v_mfma_f32_16x16x32_bf16 v[24:27], v[100:103], v[196:199], v[24:27]
	v_mfma_f32_16x16x32_bf16 v[12:15], v[60:63], v[204:207], v[12:15]
	v_mfma_f32_16x16x32_bf16 v[8:11], v[100:103], v[204:207], v[8:11]
	s_setprio 0
	s_setprio 1
	v_mfma_f32_16x16x32_bf16 v[40:43], v[120:123], v[172:175], v[40:43]
	v_mfma_f32_16x16x32_bf16 v[56:59], v[140:143], v[176:179], v[40:43]
	v_mfma_f32_16x16x32_bf16 v[40:43], v[152:155], v[172:175], v[52:55]
	v_mfma_f32_16x16x32_bf16 v[36:39], v[120:123], v[180:183], v[36:39]
	v_mfma_f32_16x16x32_bf16 v[32:35], v[152:155], v[180:183], v[32:35]
	v_mfma_f32_16x16x32_bf16 v[20:23], v[120:123], v[192:195], v[20:23]
	v_mfma_f32_16x16x32_bf16 v[16:19], v[152:155], v[192:195], v[16:19]
	v_mfma_f32_16x16x32_bf16 v[4:7], v[120:123], v[200:203], v[4:7]
	v_mfma_f32_16x16x32_bf16 v[0:3], v[152:155], v[200:203], v[0:3]
	v_mfma_f32_16x16x32_bf16 v[52:55], v[156:159], v[176:179], v[40:43]
	v_mfma_f32_16x16x32_bf16 v[36:39], v[140:143], v[184:187], v[36:39]
	v_mfma_f32_16x16x32_bf16 v[32:35], v[156:159], v[184:187], v[32:35]
	v_mfma_f32_16x16x32_bf16 v[20:23], v[140:143], v[196:199], v[20:23]
	v_mfma_f32_16x16x32_bf16 v[16:19], v[156:159], v[196:199], v[16:19]
	v_mfma_f32_16x16x32_bf16 v[4:7], v[140:143], v[204:207], v[4:7]
	v_mfma_f32_16x16x32_bf16 v[0:3], v[156:159], v[204:207], v[0:3]
	s_barrier
	s_setprio 0
	s_add_i32 s28, s28, 2
	s_add_u32 s17, s17, 0x10000
	s_addc_u32 s19, s19, 0
	s_add_u32 s0, s0, 0x100
	s_addc_u32 s1, s1, 0
	s_cmp_gt_u32 s28, 29
	s_cbranch_scc0 .LBB0_311
	s_and_b64 vcc, exec, s[34:35]
	s_cbranch_vccz .LBB0_314
	s_barrier

.LBB0_1054:
	s_ashr_i32 s41, s40, 31
	s_lshl_b64 s[4:5], s[40:41], 20
	s_add_u32 s44, s16, s4
	s_addc_u32 s45, s17, s5
	s_and_b64 s[4:5], s[36:37], exec
	s_cselect_b32 s4, s45, s51
	s_cselect_b32 s5, s44, s50
	s_ashr_i32 s39, s38, 31
	s_lshl_b64 s[46:47], s[38:39], 20
	s_add_u32 s46, s18, s46
	s_addc_u32 s47, s19, s47
	s_and_b64 s[52:53], s[36:37], exec
	s_cselect_b32 s39, s47, s1
	s_cselect_b32 s41, s46, s0
	s_add_u32 s49, s0, 0x10000
	s_addc_u32 s55, s1, 0
	s_add_u32 s0, s50, 0x80080
	s_addc_u32 s1, s51, 0
	s_mov_b32 s80, -2
	v_add_u32_e32 v140, s28, v215
	v_add_u32_e32 v156, s54, v215
	ds_read_b128 v[128:131], v140
	ds_read_b128 v[132:135], v140 offset:1024
	ds_read_b128 v[136:139], v140 offset:2048
	ds_read_b128 v[140:143], v140 offset:3072
	ds_read_b128 v[144:147], v156
	ds_read_b128 v[148:151], v156 offset:1024
	ds_read_b128 v[152:155], v156 offset:2048
	ds_read_b128 v[156:159], v156 offset:3072
	ds_read_b128 v[160:163], v251
	ds_read_b128 v[164:167], v251 offset:1024
	ds_read_b128 v[168:171], v251 offset:2048
	ds_read_b128 v[184:187], v251 offset:3072
	ds_read_b128 v[188:191], v251 offset:4096
	ds_read_b128 v[192:195], v251 offset:5120
	ds_read_b128 v[196:199], v251 offset:6144
	ds_read_b128 v[200:203], v251 offset:7168
	s_add_u32 s50, s0, 0xfff80080
	s_addc_u32 s51, s1, -1
	s_cmp_eq_u32 s80, 28
	s_cselect_b32 s53, s4, s51
	s_cselect_b32 s52, s5, s50
	s_cselect_b32 s51, s39, s55
	s_cselect_b32 s50, s41, s49
	v_lshl_add_u64 v[204:205], s[0:1], 0, v[180:181]
	s_add_i32 m0, s58, 0xc000
	s_nop 0
	global_load_lds_dwordx4 v[204:205], off
	v_lshl_add_u64 v[204:205], s[0:1], 0, v[182:183]
	s_add_i32 m0, s58, 0xe000
	s_nop 0
	global_load_lds_dwordx4 v[204:205], off
	s_waitcnt vmcnt(8)
	s_waitcnt lgkmcnt(0)
	s_setprio 1
	s_barrier
	v_mfma_f32_16x16x32_bf16 v[124:127], v[128:131], v[160:163], 0
	v_mfma_f32_16x16x32_bf16 v[120:123], v[136:139], v[160:163], 0
	v_mfma_f32_16x16x32_bf16 v[116:119], v[128:131], v[168:171], 0
	v_mfma_f32_16x16x32_bf16 v[112:115], v[136:139], v[168:171], 0
	v_mfma_f32_16x16x32_bf16 v[108:111], v[128:131], v[188:191], 0
	v_mfma_f32_16x16x32_bf16 v[104:107], v[136:139], v[188:191], 0
	v_mfma_f32_16x16x32_bf16 v[100:103], v[128:131], v[196:199], 0
	v_mfma_f32_16x16x32_bf16 v[96:99], v[136:139], v[196:199], 0
	v_mfma_f32_16x16x32_bf16 v[124:127], v[132:135], v[164:167], v[124:127]
	v_mfma_f32_16x16x32_bf16 v[120:123], v[140:143], v[164:167], v[120:123]
	v_mfma_f32_16x16x32_bf16 v[116:119], v[132:135], v[184:187], v[116:119]
	v_mfma_f32_16x16x32_bf16 v[112:115], v[140:143], v[184:187], v[112:115]
	v_mfma_f32_16x16x32_bf16 v[108:111], v[132:135], v[192:195], v[108:111]
	v_mfma_f32_16x16x32_bf16 v[104:107], v[140:143], v[192:195], v[104:107]
	v_mfma_f32_16x16x32_bf16 v[100:103], v[132:135], v[200:203], v[100:103]
	v_mfma_f32_16x16x32_bf16 v[96:99], v[140:143], v[200:203], v[96:99]
	s_setprio 0
	s_setprio 1
	v_mfma_f32_16x16x32_bf16 v[60:63], v[144:147], v[160:163], 0
	v_mfma_f32_16x16x32_bf16 v[56:59], v[152:155], v[160:163], 0
	v_mfma_f32_16x16x32_bf16 v[52:55], v[144:147], v[168:171], 0
	v_mfma_f32_16x16x32_bf16 v[48:51], v[152:155], v[168:171], 0
	v_mfma_f32_16x16x32_bf16 v[44:47], v[144:147], v[188:191], 0
	v_mfma_f32_16x16x32_bf16 v[40:43], v[152:155], v[188:191], 0
	v_mfma_f32_16x16x32_bf16 v[36:39], v[144:147], v[196:199], 0
	v_mfma_f32_16x16x32_bf16 v[32:35], v[152:155], v[196:199], 0
	v_mfma_f32_16x16x32_bf16 v[60:63], v[148:151], v[164:167], v[60:63]
	v_mfma_f32_16x16x32_bf16 v[56:59], v[156:159], v[164:167], v[56:59]
	v_mfma_f32_16x16x32_bf16 v[52:55], v[148:151], v[184:187], v[52:55]
	v_mfma_f32_16x16x32_bf16 v[48:51], v[156:159], v[184:187], v[48:51]
	v_mfma_f32_16x16x32_bf16 v[44:47], v[148:151], v[192:195], v[44:47]
	v_mfma_f32_16x16x32_bf16 v[40:43], v[156:159], v[192:195], v[40:43]
	v_mfma_f32_16x16x32_bf16 v[36:39], v[148:151], v[200:203], v[36:39]
	v_mfma_f32_16x16x32_bf16 v[32:35], v[156:159], v[200:203], v[32:35]
	s_barrier
	s_setprio 0
	ds_read_b128 v[160:163], v251 offset:16384
	ds_read_b128 v[164:167], v251 offset:17408
	ds_read_b128 v[168:171], v251 offset:18432
	ds_read_b128 v[184:187], v251 offset:19456
	ds_read_b128 v[188:191], v251 offset:20480
	ds_read_b128 v[192:195], v251 offset:21504
	ds_read_b128 v[196:199], v251 offset:22528
	ds_read_b128 v[200:203], v251 offset:23552
	s_mov_b32 m0, s30
	v_lshl_add_u64 v[204:205], s[50:51], 0, v[174:175]
	s_add_u32 s82, s50, 0x4000
	global_load_lds_dwordx4 v[204:205], off
	v_lshl_add_u64 v[204:205], s[50:51], 0, v[178:179]
	s_mov_b32 m0, s43
	s_addc_u32 s83, s51, 0
	global_load_lds_dwordx4 v[204:205], off
	v_lshl_add_u64 v[204:205], s[82:83], 0, v[174:175]
	s_mov_b32 m0, s56
	v_lshl_add_u64 v[206:207], s[52:53], 0, v[176:177]
	global_load_lds_dwordx4 v[204:205], off
	v_lshl_add_u64 v[204:205], s[82:83], 0, v[178:179]
	s_mov_b32 m0, s57
	s_nop 0
	global_load_lds_dwordx4 v[204:205], off
	v_lshl_add_u64 v[204:205], s[52:53], 0, v[172:173]
	s_mov_b32 m0, s58
	s_nop 0
	global_load_lds_dwordx4 v[204:205], off
	s_mov_b32 m0, s59
	s_nop 0
	global_load_lds_dwordx4 v[206:207], off
	s_waitcnt vmcnt(8)
	s_waitcnt lgkmcnt(0)
	s_setprio 1
	s_barrier
	v_mfma_f32_16x16x32_bf16 v[92:95], v[128:131], v[160:163], 0
	v_mfma_f32_16x16x32_bf16 v[88:91], v[136:139], v[160:163], 0
	v_mfma_f32_16x16x32_bf16 v[84:87], v[128:131], v[168:171], 0
	v_mfma_f32_16x16x32_bf16 v[80:83], v[136:139], v[168:171], 0
	v_mfma_f32_16x16x32_bf16 v[76:79], v[128:131], v[188:191], 0
	v_mfma_f32_16x16x32_bf16 v[72:75], v[136:139], v[188:191], 0
	v_mfma_f32_16x16x32_bf16 v[68:71], v[128:131], v[196:199], 0
	v_mfma_f32_16x16x32_bf16 v[64:67], v[136:139], v[196:199], 0
	v_mfma_f32_16x16x32_bf16 v[92:95], v[132:135], v[164:167], v[92:95]
	v_mfma_f32_16x16x32_bf16 v[88:91], v[140:143], v[164:167], v[88:91]
	v_mfma_f32_16x16x32_bf16 v[84:87], v[132:135], v[184:187], v[84:87]
	v_mfma_f32_16x16x32_bf16 v[80:83], v[140:143], v[184:187], v[80:83]
	v_mfma_f32_16x16x32_bf16 v[76:79], v[132:135], v[192:195], v[76:79]
	v_mfma_f32_16x16x32_bf16 v[72:75], v[140:143], v[192:195], v[72:75]
	v_mfma_f32_16x16x32_bf16 v[68:71], v[132:135], v[200:203], v[68:71]
	v_mfma_f32_16x16x32_bf16 v[64:67], v[140:143], v[200:203], v[64:67]
	s_setprio 0
	s_setprio 1
	v_mfma_f32_16x16x32_bf16 v[28:31], v[144:147], v[160:163], 0
	v_mfma_f32_16x16x32_bf16 v[24:27], v[152:155], v[160:163], 0
	v_mfma_f32_16x16x32_bf16 v[20:23], v[144:147], v[168:171], 0
	v_mfma_f32_16x16x32_bf16 v[16:19], v[152:155], v[168:171], 0
	v_mfma_f32_16x16x32_bf16 v[12:15], v[144:147], v[188:191], 0
	v_mfma_f32_16x16x32_bf16 v[8:11], v[152:155], v[188:191], 0
	v_mfma_f32_16x16x32_bf16 v[4:7], v[144:147], v[196:199], 0
	v_mfma_f32_16x16x32_bf16 v[0:3], v[152:155], v[196:199], 0
	v_mfma_f32_16x16x32_bf16 v[28:31], v[148:151], v[164:167], v[28:31]
	v_mfma_f32_16x16x32_bf16 v[24:27], v[156:159], v[164:167], v[24:27]
	v_mfma_f32_16x16x32_bf16 v[20:23], v[148:151], v[184:187], v[20:23]
	v_mfma_f32_16x16x32_bf16 v[16:19], v[156:159], v[184:187], v[16:19]
	v_mfma_f32_16x16x32_bf16 v[12:15], v[148:151], v[192:195], v[12:15]
	v_mfma_f32_16x16x32_bf16 v[8:11], v[156:159], v[192:195], v[8:11]
	v_mfma_f32_16x16x32_bf16 v[4:7], v[148:151], v[200:203], v[4:7]
	v_mfma_f32_16x16x32_bf16 v[0:3], v[156:159], v[200:203], v[0:3]
	s_barrier
	s_setprio 0
	v_add_u32_e32 v140, s68, v215
	v_add_u32_e32 v156, s73, v215
	ds_read_b128 v[128:131], v140
	ds_read_b128 v[132:135], v140 offset:1024
	ds_read_b128 v[136:139], v140 offset:2048
	ds_read_b128 v[140:143], v140 offset:3072
	ds_read_b128 v[144:147], v156
	ds_read_b128 v[148:151], v156 offset:1024
	ds_read_b128 v[152:155], v156 offset:2048
	ds_read_b128 v[156:159], v156 offset:3072
	ds_read_b128 v[160:163], v251 offset:32768
	ds_read_b128 v[164:167], v251 offset:33792
	ds_read_b128 v[168:171], v251 offset:34816
	ds_read_b128 v[184:187], v251 offset:35840
	ds_read_b128 v[188:191], v251 offset:36864
	ds_read_b128 v[192:195], v251 offset:37888
	ds_read_b128 v[196:199], v251 offset:38912
	ds_read_b128 v[200:203], v251 offset:39936
	s_add_u32 s52, s52, 0x80000
	s_addc_u32 s53, s53, 0
	s_mov_b32 m0, s60
	v_lshl_add_u64 v[208:209], s[52:53], 0, v[172:173]
	global_load_lds_dwordx4 v[208:209], off
	v_lshl_add_u64 v[208:209], s[52:53], 0, v[176:177]
	s_mov_b32 m0, s61
	s_nop 0
	global_load_lds_dwordx4 v[208:209], off
	s_waitcnt vmcnt(8)
	s_waitcnt lgkmcnt(0)
	s_setprio 1
	s_barrier
	v_mfma_f32_16x16x32_bf16 v[124:127], v[128:131], v[160:163], v[124:127]
	v_mfma_f32_16x16x32_bf16 v[120:123], v[136:139], v[160:163], v[120:123]
	v_mfma_f32_16x16x32_bf16 v[116:119], v[128:131], v[168:171], v[116:119]
	v_mfma_f32_16x16x32_bf16 v[112:115], v[136:139], v[168:171], v[112:115]
	v_mfma_f32_16x16x32_bf16 v[108:111], v[128:131], v[188:191], v[108:111]
	v_mfma_f32_16x16x32_bf16 v[104:107], v[136:139], v[188:191], v[104:107]
	v_mfma_f32_16x16x32_bf16 v[100:103], v[128:131], v[196:199], v[100:103]
	v_mfma_f32_16x16x32_bf16 v[96:99], v[136:139], v[196:199], v[96:99]
	v_mfma_f32_16x16x32_bf16 v[124:127], v[132:135], v[164:167], v[124:127]
	v_mfma_f32_16x16x32_bf16 v[120:123], v[140:143], v[164:167], v[120:123]
	v_mfma_f32_16x16x32_bf16 v[116:119], v[132:135], v[184:187], v[116:119]
	v_mfma_f32_16x16x32_bf16 v[112:115], v[140:143], v[184:187], v[112:115]
	v_mfma_f32_16x16x32_bf16 v[108:111], v[132:135], v[192:195], v[108:111]
	v_mfma_f32_16x16x32_bf16 v[104:107], v[140:143], v[192:195], v[104:107]
	v_mfma_f32_16x16x32_bf16 v[100:103], v[132:135], v[200:203], v[100:103]
	v_mfma_f32_16x16x32_bf16 v[96:99], v[140:143], v[200:203], v[96:99]
	s_setprio 0
	s_setprio 1
	v_mfma_f32_16x16x32_bf16 v[60:63], v[144:147], v[160:163], v[60:63]
	v_mfma_f32_16x16x32_bf16 v[56:59], v[152:155], v[160:163], v[56:59]
	v_mfma_f32_16x16x32_bf16 v[52:55], v[144:147], v[168:171], v[52:55]
	v_mfma_f32_16x16x32_bf16 v[48:51], v[152:155], v[168:171], v[48:51]
	v_mfma_f32_16x16x32_bf16 v[44:47], v[144:147], v[188:191], v[44:47]
	v_mfma_f32_16x16x32_bf16 v[40:43], v[152:155], v[188:191], v[40:43]
	v_mfma_f32_16x16x32_bf16 v[36:39], v[144:147], v[196:199], v[36:39]
	v_mfma_f32_16x16x32_bf16 v[32:35], v[152:155], v[196:199], v[32:35]
	v_mfma_f32_16x16x32_bf16 v[60:63], v[148:151], v[164:167], v[60:63]
	v_mfma_f32_16x16x32_bf16 v[56:59], v[156:159], v[164:167], v[56:59]
	v_mfma_f32_16x16x32_bf16 v[52:55], v[148:151], v[184:187], v[52:55]
	v_mfma_f32_16x16x32_bf16 v[48:51], v[156:159], v[184:187], v[48:51]
	v_mfma_f32_16x16x32_bf16 v[44:47], v[148:151], v[192:195], v[44:47]
	v_mfma_f32_16x16x32_bf16 v[40:43], v[156:159], v[192:195], v[40:43]
	v_mfma_f32_16x16x32_bf16 v[36:39], v[148:151], v[200:203], v[36:39]
	v_mfma_f32_16x16x32_bf16 v[32:35], v[156:159], v[200:203], v[32:35]
	s_barrier
	s_setprio 0
	ds_read_b128 v[160:163], v251 offset:49152
	ds_read_b128 v[164:167], v251 offset:50176
	ds_read_b128 v[168:171], v251 offset:51200
	ds_read_b128 v[184:187], v251 offset:52224
	ds_read_b128 v[188:191], v251 offset:53248
	ds_read_b128 v[192:195], v251 offset:54272
	ds_read_b128 v[196:199], v251 offset:55296
	ds_read_b128 v[200:203], v251 offset:56320
	s_add_u32 s52, s50, 0x8000
	s_addc_u32 s53, s51, 0
	s_mov_b32 m0, s69
	v_lshl_add_u64 v[208:209], s[52:53], 0, v[174:175]
	s_add_u32 s50, s50, 0xc000
	global_load_lds_dwordx4 v[208:209], off
	v_lshl_add_u64 v[208:209], s[52:53], 0, v[178:179]
	s_mov_b32 m0, s70
	s_addc_u32 s51, s51, 0
	global_load_lds_dwordx4 v[208:209], off
	v_lshl_add_u64 v[208:209], s[50:51], 0, v[174:175]
	s_mov_b32 m0, s74
	v_lshl_add_u64 v[204:205], v[204:205], 0, s[26:27]
	global_load_lds_dwordx4 v[208:209], off
	v_lshl_add_u64 v[208:209], s[50:51], 0, v[178:179]
	s_mov_b32 m0, s75
	s_nop 0
	global_load_lds_dwordx4 v[208:209], off
	s_mov_b32 m0, s71
	s_nop 0
	global_load_lds_dwordx4 v[204:205], off
	v_lshl_add_u64 v[204:205], v[206:207], 0, s[26:27]
	s_mov_b32 m0, s72
	s_nop 0
	global_load_lds_dwordx4 v[204:205], off
	s_waitcnt vmcnt(8)
	s_waitcnt lgkmcnt(0)
	s_setprio 1
	s_barrier
	v_mfma_f32_16x16x32_bf16 v[92:95], v[128:131], v[160:163], v[92:95]
	v_mfma_f32_16x16x32_bf16 v[88:91], v[136:139], v[160:163], v[88:91]
	v_mfma_f32_16x16x32_bf16 v[84:87], v[128:131], v[168:171], v[84:87]
	v_mfma_f32_16x16x32_bf16 v[80:83], v[136:139], v[168:171], v[80:83]
	v_mfma_f32_16x16x32_bf16 v[76:79], v[128:131], v[188:191], v[76:79]
	v_mfma_f32_16x16x32_bf16 v[72:75], v[136:139], v[188:191], v[72:75]
	v_mfma_f32_16x16x32_bf16 v[68:71], v[128:131], v[196:199], v[68:71]
	v_mfma_f32_16x16x32_bf16 v[64:67], v[136:139], v[196:199], v[64:67]
	v_mfma_f32_16x16x32_bf16 v[92:95], v[132:135], v[164:167], v[92:95]
	v_mfma_f32_16x16x32_bf16 v[88:91], v[140:143], v[164:167], v[88:91]
	v_mfma_f32_16x16x32_bf16 v[84:87], v[132:135], v[184:187], v[84:87]
	v_mfma_f32_16x16x32_bf16 v[80:83], v[140:143], v[184:187], v[80:83]
	v_mfma_f32_16x16x32_bf16 v[76:79], v[132:135], v[192:195], v[76:79]
	v_mfma_f32_16x16x32_bf16 v[72:75], v[140:143], v[192:195], v[72:75]
	v_mfma_f32_16x16x32_bf16 v[68:71], v[132:135], v[200:203], v[68:71]
	v_mfma_f32_16x16x32_bf16 v[64:67], v[140:143], v[200:203], v[64:67]
	s_setprio 0
	s_setprio 1
	v_mfma_f32_16x16x32_bf16 v[28:31], v[144:147], v[160:163], v[28:31]
	v_mfma_f32_16x16x32_bf16 v[24:27], v[152:155], v[160:163], v[24:27]
	v_mfma_f32_16x16x32_bf16 v[20:23], v[144:147], v[168:171], v[20:23]
	v_mfma_f32_16x16x32_bf16 v[16:19], v[152:155], v[168:171], v[16:19]
	v_mfma_f32_16x16x32_bf16 v[12:15], v[144:147], v[188:191], v[12:15]
	v_mfma_f32_16x16x32_bf16 v[8:11], v[152:155], v[188:191], v[8:11]
	v_mfma_f32_16x16x32_bf16 v[4:7], v[144:147], v[196:199], v[4:7]
	v_mfma_f32_16x16x32_bf16 v[0:3], v[152:155], v[196:199], v[0:3]
	v_mfma_f32_16x16x32_bf16 v[28:31], v[148:151], v[164:167], v[28:31]
	v_mfma_f32_16x16x32_bf16 v[24:27], v[156:159], v[164:167], v[24:27]
	v_mfma_f32_16x16x32_bf16 v[20:23], v[148:151], v[184:187], v[20:23]
	v_mfma_f32_16x16x32_bf16 v[16:19], v[156:159], v[184:187], v[16:19]
	v_mfma_f32_16x16x32_bf16 v[12:15], v[148:151], v[192:195], v[12:15]
	v_mfma_f32_16x16x32_bf16 v[8:11], v[156:159], v[192:195], v[8:11]
	v_mfma_f32_16x16x32_bf16 v[4:7], v[148:151], v[200:203], v[4:7]
	v_mfma_f32_16x16x32_bf16 v[0:3], v[156:159], v[200:203], v[0:3]
	s_barrier
	s_setprio 0
	s_add_i32 s80, s80, 2
	s_add_u32 s49, s49, 0x10000
	s_addc_u32 s55, s55, 0
	s_add_u32 s0, s0, 0x100
	s_addc_u32 s1, s1, 0
	s_cmp_gt_u32 s80, 29
.LBB0_1055:
	v_add_u32_e32 v140, s28, v215
	v_add_u32_e32 v156, s54, v215
	ds_read_b128 v[128:131], v140
	ds_read_b128 v[132:135], v140 offset:1024
	ds_read_b128 v[136:139], v140 offset:2048
	ds_read_b128 v[140:143], v140 offset:3072
	ds_read_b128 v[144:147], v156
	ds_read_b128 v[148:151], v156 offset:1024
	ds_read_b128 v[152:155], v156 offset:2048
	ds_read_b128 v[156:159], v156 offset:3072
	ds_read_b128 v[160:163], v251
	ds_read_b128 v[164:167], v251 offset:1024
	ds_read_b128 v[168:171], v251 offset:2048
	ds_read_b128 v[184:187], v251 offset:3072
	ds_read_b128 v[188:191], v251 offset:4096
	ds_read_b128 v[192:195], v251 offset:5120
	ds_read_b128 v[196:199], v251 offset:6144
	ds_read_b128 v[200:203], v251 offset:7168
	s_add_u32 s50, s0, 0xfff80080
	s_addc_u32 s51, s1, -1
	s_cmp_eq_u32 s80, 28
	s_cselect_b32 s53, s4, s51
	s_cselect_b32 s52, s5, s50
	s_cselect_b32 s51, s39, s55
	s_cselect_b32 s50, s41, s49
	v_lshl_add_u64 v[204:205], s[0:1], 0, v[180:181]
	s_add_i32 m0, s58, 0xc000
	s_nop 0
	global_load_lds_dwordx4 v[204:205], off
	v_lshl_add_u64 v[204:205], s[0:1], 0, v[182:183]
	s_add_i32 m0, s58, 0xe000
	s_nop 0
	global_load_lds_dwordx4 v[204:205], off
	s_waitcnt vmcnt(8)
	s_waitcnt lgkmcnt(0)
	s_setprio 1
	s_barrier
	v_mfma_f32_16x16x32_bf16 v[124:127], v[128:131], v[160:163], v[124:127]
	v_mfma_f32_16x16x32_bf16 v[120:123], v[136:139], v[160:163], v[120:123]
	v_mfma_f32_16x16x32_bf16 v[116:119], v[128:131], v[168:171], v[116:119]
	v_mfma_f32_16x16x32_bf16 v[112:115], v[136:139], v[168:171], v[112:115]
	v_mfma_f32_16x16x32_bf16 v[108:111], v[128:131], v[188:191], v[108:111]
	v_mfma_f32_16x16x32_bf16 v[104:107], v[136:139], v[188:191], v[104:107]
	v_mfma_f32_16x16x32_bf16 v[100:103], v[128:131], v[196:199], v[100:103]
	v_mfma_f32_16x16x32_bf16 v[96:99], v[136:139], v[196:199], v[96:99]
	v_mfma_f32_16x16x32_bf16 v[124:127], v[132:135], v[164:167], v[124:127]
	v_mfma_f32_16x16x32_bf16 v[120:123], v[140:143], v[164:167], v[120:123]
	v_mfma_f32_16x16x32_bf16 v[116:119], v[132:135], v[184:187], v[116:119]
	v_mfma_f32_16x16x32_bf16 v[112:115], v[140:143], v[184:187], v[112:115]
	v_mfma_f32_16x16x32_bf16 v[108:111], v[132:135], v[192:195], v[108:111]
	v_mfma_f32_16x16x32_bf16 v[104:107], v[140:143], v[192:195], v[104:107]
	v_mfma_f32_16x16x32_bf16 v[100:103], v[132:135], v[200:203], v[100:103]
	v_mfma_f32_16x16x32_bf16 v[96:99], v[140:143], v[200:203], v[96:99]
	s_setprio 0
	s_setprio 1
	v_mfma_f32_16x16x32_bf16 v[60:63], v[144:147], v[160:163], v[60:63]
	v_mfma_f32_16x16x32_bf16 v[56:59], v[152:155], v[160:163], v[56:59]
	v_mfma_f32_16x16x32_bf16 v[52:55], v[144:147], v[168:171], v[52:55]
	v_mfma_f32_16x16x32_bf16 v[48:51], v[152:155], v[168:171], v[48:51]
	v_mfma_f32_16x16x32_bf16 v[44:47], v[144:147], v[188:191], v[44:47]
	v_mfma_f32_16x16x32_bf16 v[40:43], v[152:155], v[188:191], v[40:43]
	v_mfma_f32_16x16x32_bf16 v[36:39], v[144:147], v[196:199], v[36:39]
	v_mfma_f32_16x16x32_bf16 v[32:35], v[152:155], v[196:199], v[32:35]
	v_mfma_f32_16x16x32_bf16 v[60:63], v[148:151], v[164:167], v[60:63]
	v_mfma_f32_16x16x32_bf16 v[56:59], v[156:159], v[164:167], v[56:59]
	v_mfma_f32_16x16x32_bf16 v[52:55], v[148:151], v[184:187], v[52:55]
	v_mfma_f32_16x16x32_bf16 v[48:51], v[156:159], v[184:187], v[48:51]
	v_mfma_f32_16x16x32_bf16 v[44:47], v[148:151], v[192:195], v[44:47]
	v_mfma_f32_16x16x32_bf16 v[40:43], v[156:159], v[192:195], v[40:43]
	v_mfma_f32_16x16x32_bf16 v[36:39], v[148:151], v[200:203], v[36:39]
	v_mfma_f32_16x16x32_bf16 v[32:35], v[156:159], v[200:203], v[32:35]
	s_barrier
	s_setprio 0
	ds_read_b128 v[160:163], v251 offset:16384
	ds_read_b128 v[164:167], v251 offset:17408
	ds_read_b128 v[168:171], v251 offset:18432
	ds_read_b128 v[184:187], v251 offset:19456
	ds_read_b128 v[188:191], v251 offset:20480
	ds_read_b128 v[192:195], v251 offset:21504
	ds_read_b128 v[196:199], v251 offset:22528
	ds_read_b128 v[200:203], v251 offset:23552
	s_mov_b32 m0, s30
	v_lshl_add_u64 v[204:205], s[50:51], 0, v[174:175]
	s_add_u32 s82, s50, 0x4000
	global_load_lds_dwordx4 v[204:205], off
	v_lshl_add_u64 v[204:205], s[50:51], 0, v[178:179]
	s_mov_b32 m0, s43
	s_addc_u32 s83, s51, 0
	global_load_lds_dwordx4 v[204:205], off
	v_lshl_add_u64 v[204:205], s[82:83], 0, v[174:175]
	s_mov_b32 m0, s56
	v_lshl_add_u64 v[206:207], s[52:53], 0, v[176:177]
	global_load_lds_dwordx4 v[204:205], off
	v_lshl_add_u64 v[204:205], s[82:83], 0, v[178:179]
	s_mov_b32 m0, s57
	s_nop 0
	global_load_lds_dwordx4 v[204:205], off
	v_lshl_add_u64 v[204:205], s[52:53], 0, v[172:173]
	s_mov_b32 m0, s58
	s_nop 0
	global_load_lds_dwordx4 v[204:205], off
	s_mov_b32 m0, s59
	s_nop 0
	global_load_lds_dwordx4 v[206:207], off
	s_waitcnt vmcnt(8)
	s_waitcnt lgkmcnt(0)
	s_setprio 1
	s_barrier
	v_mfma_f32_16x16x32_bf16 v[92:95], v[128:131], v[160:163], v[92:95]
	v_mfma_f32_16x16x32_bf16 v[88:91], v[136:139], v[160:163], v[88:91]
	v_mfma_f32_16x16x32_bf16 v[84:87], v[128:131], v[168:171], v[84:87]
	v_mfma_f32_16x16x32_bf16 v[80:83], v[136:139], v[168:171], v[80:83]
	v_mfma_f32_16x16x32_bf16 v[76:79], v[128:131], v[188:191], v[76:79]
	v_mfma_f32_16x16x32_bf16 v[72:75], v[136:139], v[188:191], v[72:75]
	v_mfma_f32_16x16x32_bf16 v[68:71], v[128:131], v[196:199], v[68:71]
	v_mfma_f32_16x16x32_bf16 v[64:67], v[136:139], v[196:199], v[64:67]
	v_mfma_f32_16x16x32_bf16 v[92:95], v[132:135], v[164:167], v[92:95]
	v_mfma_f32_16x16x32_bf16 v[88:91], v[140:143], v[164:167], v[88:91]
	v_mfma_f32_16x16x32_bf16 v[84:87], v[132:135], v[184:187], v[84:87]
	v_mfma_f32_16x16x32_bf16 v[80:83], v[140:143], v[184:187], v[80:83]
	v_mfma_f32_16x16x32_bf16 v[76:79], v[132:135], v[192:195], v[76:79]
	v_mfma_f32_16x16x32_bf16 v[72:75], v[140:143], v[192:195], v[72:75]
	v_mfma_f32_16x16x32_bf16 v[68:71], v[132:135], v[200:203], v[68:71]
	v_mfma_f32_16x16x32_bf16 v[64:67], v[140:143], v[200:203], v[64:67]
	s_setprio 0
	s_setprio 1
	v_mfma_f32_16x16x32_bf16 v[28:31], v[144:147], v[160:163], v[28:31]
	v_mfma_f32_16x16x32_bf16 v[24:27], v[152:155], v[160:163], v[24:27]
	v_mfma_f32_16x16x32_bf16 v[20:23], v[144:147], v[168:171], v[20:23]
	v_mfma_f32_16x16x32_bf16 v[16:19], v[152:155], v[168:171], v[16:19]
	v_mfma_f32_16x16x32_bf16 v[12:15], v[144:147], v[188:191], v[12:15]
	v_mfma_f32_16x16x32_bf16 v[8:11], v[152:155], v[188:191], v[8:11]
	v_mfma_f32_16x16x32_bf16 v[4:7], v[144:147], v[196:199], v[4:7]
	v_mfma_f32_16x16x32_bf16 v[0:3], v[152:155], v[196:199], v[0:3]
	v_mfma_f32_16x16x32_bf16 v[28:31], v[148:151], v[164:167], v[28:31]
	v_mfma_f32_16x16x32_bf16 v[24:27], v[156:159], v[164:167], v[24:27]
	v_mfma_f32_16x16x32_bf16 v[20:23], v[148:151], v[184:187], v[20:23]
	v_mfma_f32_16x16x32_bf16 v[16:19], v[156:159], v[184:187], v[16:19]
	v_mfma_f32_16x16x32_bf16 v[12:15], v[148:151], v[192:195], v[12:15]
	v_mfma_f32_16x16x32_bf16 v[8:11], v[156:159], v[192:195], v[8:11]
	v_mfma_f32_16x16x32_bf16 v[4:7], v[148:151], v[200:203], v[4:7]
	v_mfma_f32_16x16x32_bf16 v[0:3], v[156:159], v[200:203], v[0:3]
	s_barrier
	s_setprio 0
	v_add_u32_e32 v140, s68, v215
	v_add_u32_e32 v156, s73, v215
	ds_read_b128 v[128:131], v140
	ds_read_b128 v[132:135], v140 offset:1024
	ds_read_b128 v[136:139], v140 offset:2048
	ds_read_b128 v[140:143], v140 offset:3072
	ds_read_b128 v[144:147], v156
	ds_read_b128 v[148:151], v156 offset:1024
	ds_read_b128 v[152:155], v156 offset:2048
	ds_read_b128 v[156:159], v156 offset:3072
	ds_read_b128 v[160:163], v251 offset:32768
	ds_read_b128 v[164:167], v251 offset:33792
	ds_read_b128 v[168:171], v251 offset:34816
	ds_read_b128 v[184:187], v251 offset:35840
	ds_read_b128 v[188:191], v251 offset:36864
	ds_read_b128 v[192:195], v251 offset:37888
	ds_read_b128 v[196:199], v251 offset:38912
	ds_read_b128 v[200:203], v251 offset:39936
	s_add_u32 s52, s52, 0x80000
	s_addc_u32 s53, s53, 0
	s_mov_b32 m0, s60
	v_lshl_add_u64 v[208:209], s[52:53], 0, v[172:173]
	global_load_lds_dwordx4 v[208:209], off
	v_lshl_add_u64 v[208:209], s[52:53], 0, v[176:177]
	s_mov_b32 m0, s61
	s_nop 0
	global_load_lds_dwordx4 v[208:209], off
	s_waitcnt vmcnt(8)
	s_waitcnt lgkmcnt(0)
	s_setprio 1
	s_barrier
	v_mfma_f32_16x16x32_bf16 v[124:127], v[128:131], v[160:163], v[124:127]
	v_mfma_f32_16x16x32_bf16 v[120:123], v[136:139], v[160:163], v[120:123]
	v_mfma_f32_16x16x32_bf16 v[116:119], v[128:131], v[168:171], v[116:119]
	v_mfma_f32_16x16x32_bf16 v[112:115], v[136:139], v[168:171], v[112:115]
	v_mfma_f32_16x16x32_bf16 v[108:111], v[128:131], v[188:191], v[108:111]
	v_mfma_f32_16x16x32_bf16 v[104:107], v[136:139], v[188:191], v[104:107]
	v_mfma_f32_16x16x32_bf16 v[100:103], v[128:131], v[196:199], v[100:103]
	v_mfma_f32_16x16x32_bf16 v[96:99], v[136:139], v[196:199], v[96:99]
	v_mfma_f32_16x16x32_bf16 v[124:127], v[132:135], v[164:167], v[124:127]
	v_mfma_f32_16x16x32_bf16 v[120:123], v[140:143], v[164:167], v[120:123]
	v_mfma_f32_16x16x32_bf16 v[116:119], v[132:135], v[184:187], v[116:119]
	v_mfma_f32_16x16x32_bf16 v[112:115], v[140:143], v[184:187], v[112:115]
	v_mfma_f32_16x16x32_bf16 v[108:111], v[132:135], v[192:195], v[108:111]
	v_mfma_f32_16x16x32_bf16 v[104:107], v[140:143], v[192:195], v[104:107]
	v_mfma_f32_16x16x32_bf16 v[100:103], v[132:135], v[200:203], v[100:103]
	v_mfma_f32_16x16x32_bf16 v[96:99], v[140:143], v[200:203], v[96:99]
	s_setprio 0
	s_setprio 1
	v_mfma_f32_16x16x32_bf16 v[60:63], v[144:147], v[160:163], v[60:63]
	v_mfma_f32_16x16x32_bf16 v[56:59], v[152:155], v[160:163], v[56:59]
	v_mfma_f32_16x16x32_bf16 v[52:55], v[144:147], v[168:171], v[52:55]
	v_mfma_f32_16x16x32_bf16 v[48:51], v[152:155], v[168:171], v[48:51]
	v_mfma_f32_16x16x32_bf16 v[44:47], v[144:147], v[188:191], v[44:47]
	v_mfma_f32_16x16x32_bf16 v[40:43], v[152:155], v[188:191], v[40:43]
	v_mfma_f32_16x16x32_bf16 v[36:39], v[144:147], v[196:199], v[36:39]
	v_mfma_f32_16x16x32_bf16 v[32:35], v[152:155], v[196:199], v[32:35]
	v_mfma_f32_16x16x32_bf16 v[60:63], v[148:151], v[164:167], v[60:63]
	v_mfma_f32_16x16x32_bf16 v[56:59], v[156:159], v[164:167], v[56:59]
	v_mfma_f32_16x16x32_bf16 v[52:55], v[148:151], v[184:187], v[52:55]
	v_mfma_f32_16x16x32_bf16 v[48:51], v[156:159], v[184:187], v[48:51]
	v_mfma_f32_16x16x32_bf16 v[44:47], v[148:151], v[192:195], v[44:47]
	v_mfma_f32_16x16x32_bf16 v[40:43], v[156:159], v[192:195], v[40:43]
	v_mfma_f32_16x16x32_bf16 v[36:39], v[148:151], v[200:203], v[36:39]
	v_mfma_f32_16x16x32_bf16 v[32:35], v[156:159], v[200:203], v[32:35]
	s_barrier
	s_setprio 0
	ds_read_b128 v[160:163], v251 offset:49152
	ds_read_b128 v[164:167], v251 offset:50176
	ds_read_b128 v[168:171], v251 offset:51200
	ds_read_b128 v[184:187], v251 offset:52224
	ds_read_b128 v[188:191], v251 offset:53248
	ds_read_b128 v[192:195], v251 offset:54272
	ds_read_b128 v[196:199], v251 offset:55296
	ds_read_b128 v[200:203], v251 offset:56320
	s_add_u32 s52, s50, 0x8000
	s_addc_u32 s53, s51, 0
	s_mov_b32 m0, s69
	v_lshl_add_u64 v[208:209], s[52:53], 0, v[174:175]
	s_add_u32 s50, s50, 0xc000
	global_load_lds_dwordx4 v[208:209], off
	v_lshl_add_u64 v[208:209], s[52:53], 0, v[178:179]
	s_mov_b32 m0, s70
	s_addc_u32 s51, s51, 0
	global_load_lds_dwordx4 v[208:209], off
	v_lshl_add_u64 v[208:209], s[50:51], 0, v[174:175]
	s_mov_b32 m0, s74
	v_lshl_add_u64 v[204:205], v[204:205], 0, s[26:27]
	global_load_lds_dwordx4 v[208:209], off
	v_lshl_add_u64 v[208:209], s[50:51], 0, v[178:179]
	s_mov_b32 m0, s75
	s_nop 0
	global_load_lds_dwordx4 v[208:209], off
	s_mov_b32 m0, s71
	s_nop 0
	global_load_lds_dwordx4 v[204:205], off
	v_lshl_add_u64 v[204:205], v[206:207], 0, s[26:27]
	s_mov_b32 m0, s72
	s_nop 0
	global_load_lds_dwordx4 v[204:205], off
	s_waitcnt vmcnt(8)
	s_waitcnt lgkmcnt(0)
	s_setprio 1
	s_barrier
	v_mfma_f32_16x16x32_bf16 v[92:95], v[128:131], v[160:163], v[92:95]
	v_mfma_f32_16x16x32_bf16 v[88:91], v[136:139], v[160:163], v[88:91]
	v_mfma_f32_16x16x32_bf16 v[84:87], v[128:131], v[168:171], v[84:87]
	v_mfma_f32_16x16x32_bf16 v[80:83], v[136:139], v[168:171], v[80:83]
	v_mfma_f32_16x16x32_bf16 v[76:79], v[128:131], v[188:191], v[76:79]
	v_mfma_f32_16x16x32_bf16 v[72:75], v[136:139], v[188:191], v[72:75]
	v_mfma_f32_16x16x32_bf16 v[68:71], v[128:131], v[196:199], v[68:71]
	v_mfma_f32_16x16x32_bf16 v[64:67], v[136:139], v[196:199], v[64:67]
	v_mfma_f32_16x16x32_bf16 v[92:95], v[132:135], v[164:167], v[92:95]
	v_mfma_f32_16x16x32_bf16 v[88:91], v[140:143], v[164:167], v[88:91]
	v_mfma_f32_16x16x32_bf16 v[84:87], v[132:135], v[184:187], v[84:87]
	v_mfma_f32_16x16x32_bf16 v[80:83], v[140:143], v[184:187], v[80:83]
	v_mfma_f32_16x16x32_bf16 v[76:79], v[132:135], v[192:195], v[76:79]
	v_mfma_f32_16x16x32_bf16 v[72:75], v[140:143], v[192:195], v[72:75]
	v_mfma_f32_16x16x32_bf16 v[68:71], v[132:135], v[200:203], v[68:71]
	v_mfma_f32_16x16x32_bf16 v[64:67], v[140:143], v[200:203], v[64:67]
	s_setprio 0
	s_setprio 1
	v_mfma_f32_16x16x32_bf16 v[28:31], v[144:147], v[160:163], v[28:31]
	v_mfma_f32_16x16x32_bf16 v[24:27], v[152:155], v[160:163], v[24:27]
	v_mfma_f32_16x16x32_bf16 v[20:23], v[144:147], v[168:171], v[20:23]
	v_mfma_f32_16x16x32_bf16 v[16:19], v[152:155], v[168:171], v[16:19]
	v_mfma_f32_16x16x32_bf16 v[12:15], v[144:147], v[188:191], v[12:15]
	v_mfma_f32_16x16x32_bf16 v[8:11], v[152:155], v[188:191], v[8:11]
	v_mfma_f32_16x16x32_bf16 v[4:7], v[144:147], v[196:199], v[4:7]
	v_mfma_f32_16x16x32_bf16 v[0:3], v[152:155], v[196:199], v[0:3]
	v_mfma_f32_16x16x32_bf16 v[28:31], v[148:151], v[164:167], v[28:31]
	v_mfma_f32_16x16x32_bf16 v[24:27], v[156:159], v[164:167], v[24:27]
	v_mfma_f32_16x16x32_bf16 v[20:23], v[148:151], v[184:187], v[20:23]
	v_mfma_f32_16x16x32_bf16 v[16:19], v[156:159], v[184:187], v[16:19]
	v_mfma_f32_16x16x32_bf16 v[12:15], v[148:151], v[192:195], v[12:15]
	v_mfma_f32_16x16x32_bf16 v[8:11], v[156:159], v[192:195], v[8:11]
	v_mfma_f32_16x16x32_bf16 v[4:7], v[148:151], v[200:203], v[4:7]
	v_mfma_f32_16x16x32_bf16 v[0:3], v[156:159], v[200:203], v[0:3]
	s_barrier
	s_setprio 0
	s_add_i32 s80, s80, 2
	s_add_u32 s49, s49, 0x10000
	s_addc_u32 s55, s55, 0
	s_add_u32 s0, s0, 0x100
	s_addc_u32 s1, s1, 0
	s_cmp_gt_u32 s80, 29
	s_cbranch_scc0 .LBB0_1055
	v_mov_b64_e32 v[220:221], 0x1ff
	v_mov_b64_e32 v[218:219], 0x200
	s_and_b64 vcc, exec, s[34:35]
	s_cbranch_vccz .LBB0_1058
	s_barrier

.LBB0_1172:
	s_ashr_i32 s39, s38, 31
	s_lshl_b64 s[4:5], s[38:39], 20
	s_add_u32 s40, s18, s4
	s_addc_u32 s41, s19, s5
	s_and_b64 s[4:5], s[36:37], exec
	s_cselect_b32 s4, s41, s1
	s_cselect_b32 s5, s40, s0
	s_ashr_i32 s35, s34, 31
	s_lshl_b64 s[42:43], s[34:35], 20
	s_add_u32 s42, s16, s42
	s_addc_u32 s43, s17, s43
	s_and_b64 s[48:49], s[36:37], exec
	s_cselect_b32 s35, s43, s47
	s_cselect_b32 s39, s42, s46
	s_add_u32 s76, s46, 0x10000
	s_addc_u32 s77, s47, 0
	s_mov_b32 s78, -2
	v_add_u32_e32 v124, s28, v156
	v_add_u32_e32 v170, s45, v156
	ds_read_b128 v[108:111], v124
	ds_read_b128 v[112:115], v124 offset:1024
	ds_read_b128 v[120:123], v124 offset:2048
	ds_read_b128 v[124:127], v124 offset:3072
	ds_read_b128 v[158:161], v170
	ds_read_b128 v[162:165], v170 offset:1024
	ds_read_b128 v[166:169], v170 offset:2048
	ds_read_b128 v[170:173], v170 offset:3072
	ds_read_b128 v[174:177], v157
	ds_read_b128 v[178:181], v157 offset:1024
	ds_read_b128 v[182:185], v157 offset:2048
	ds_read_b128 v[186:189], v157 offset:3072
	ds_read_b128 v[190:193], v157 offset:4096
	ds_read_b128 v[194:197], v157 offset:5120
	ds_read_b128 v[198:201], v157 offset:6144
	ds_read_b128 v[202:205], v157 offset:7168
	s_add_u32 s46, s0, 0x10000
	s_addc_u32 s47, s1, 0
	s_cmp_eq_u32 s78, 28
	s_cselect_b32 s52, s5, s46
	s_cselect_b32 s53, s4, s47
	s_cselect_b32 s50, s39, s76
	s_cselect_b32 s51, s35, s77
	s_add_u32 s48, s52, 0x8000
	s_addc_u32 s49, s53, 0
	v_lshl_add_u64 v[206:207], s[0:1], 0, v[152:153]
	s_add_i32 m0, s56, 0xc000
	s_nop 0
	global_load_lds_dwordx4 v[206:207], off
	v_lshl_add_u64 v[206:207], s[0:1], 0, v[154:155]
	s_add_i32 m0, s56, 0xe000
	s_nop 0
	global_load_lds_dwordx4 v[206:207], off
	s_waitcnt vmcnt(8)
	s_waitcnt lgkmcnt(0)
	s_setprio 1
	s_barrier
	v_mfma_f32_16x16x32_bf16 v[140:143], v[108:111], v[174:177], 0
	v_mfma_f32_16x16x32_bf16 v[136:139], v[120:123], v[174:177], 0
	v_mfma_f32_16x16x32_bf16 v[116:119], v[108:111], v[182:185], 0
	v_mfma_f32_16x16x32_bf16 v[104:107], v[120:123], v[182:185], 0
	v_mfma_f32_16x16x32_bf16 v[92:95], v[108:111], v[190:193], 0
	v_mfma_f32_16x16x32_bf16 v[88:91], v[120:123], v[190:193], 0
	v_mfma_f32_16x16x32_bf16 v[76:79], v[108:111], v[198:201], 0
	v_mfma_f32_16x16x32_bf16 v[72:75], v[120:123], v[198:201], 0
	v_mfma_f32_16x16x32_bf16 v[140:143], v[112:115], v[178:181], v[140:143]
	v_mfma_f32_16x16x32_bf16 v[136:139], v[124:127], v[178:181], v[136:139]
	v_mfma_f32_16x16x32_bf16 v[116:119], v[112:115], v[186:189], v[116:119]
	v_mfma_f32_16x16x32_bf16 v[104:107], v[124:127], v[186:189], v[104:107]
	v_mfma_f32_16x16x32_bf16 v[92:95], v[112:115], v[194:197], v[92:95]
	v_mfma_f32_16x16x32_bf16 v[88:91], v[124:127], v[194:197], v[88:91]
	v_mfma_f32_16x16x32_bf16 v[76:79], v[112:115], v[202:205], v[76:79]
	v_mfma_f32_16x16x32_bf16 v[72:75], v[124:127], v[202:205], v[72:75]
	s_setprio 0
	s_setprio 1
	v_mfma_f32_16x16x32_bf16 v[132:135], v[158:161], v[174:177], 0
	v_mfma_f32_16x16x32_bf16 v[128:131], v[166:169], v[174:177], 0
	v_mfma_f32_16x16x32_bf16 v[100:103], v[158:161], v[182:185], 0
	v_mfma_f32_16x16x32_bf16 v[96:99], v[166:169], v[182:185], 0
	v_mfma_f32_16x16x32_bf16 v[84:87], v[158:161], v[190:193], 0
	v_mfma_f32_16x16x32_bf16 v[80:83], v[166:169], v[190:193], 0
	v_mfma_f32_16x16x32_bf16 v[68:71], v[158:161], v[198:201], 0
	v_mfma_f32_16x16x32_bf16 v[64:67], v[166:169], v[198:201], 0
	v_mfma_f32_16x16x32_bf16 v[132:135], v[162:165], v[178:181], v[132:135]
	v_mfma_f32_16x16x32_bf16 v[128:131], v[170:173], v[178:181], v[128:131]
	v_mfma_f32_16x16x32_bf16 v[100:103], v[162:165], v[186:189], v[100:103]
	v_mfma_f32_16x16x32_bf16 v[96:99], v[170:173], v[186:189], v[96:99]
	v_mfma_f32_16x16x32_bf16 v[84:87], v[162:165], v[194:197], v[84:87]
	v_mfma_f32_16x16x32_bf16 v[80:83], v[170:173], v[194:197], v[80:83]
	v_mfma_f32_16x16x32_bf16 v[68:71], v[162:165], v[202:205], v[68:71]
	v_mfma_f32_16x16x32_bf16 v[64:67], v[170:173], v[202:205], v[64:67]
	s_barrier
	s_setprio 0
	ds_read_b128 v[174:177], v157 offset:16384
	ds_read_b128 v[178:181], v157 offset:17408
	ds_read_b128 v[182:185], v157 offset:18432
	ds_read_b128 v[186:189], v157 offset:19456
	ds_read_b128 v[190:193], v157 offset:20480
	ds_read_b128 v[194:197], v157 offset:21504
	ds_read_b128 v[198:201], v157 offset:22528
	ds_read_b128 v[202:205], v157 offset:23552
	s_mov_b32 m0, s30
	v_lshl_add_u64 v[206:207], s[50:51], 0, v[146:147]
	s_add_u32 s0, s50, 0x4000
	global_load_lds_dwordx4 v[206:207], off
	v_lshl_add_u64 v[206:207], s[50:51], 0, v[150:151]
	s_mov_b32 m0, s31
	s_addc_u32 s1, s51, 0
	global_load_lds_dwordx4 v[206:207], off
	v_lshl_add_u64 v[206:207], s[0:1], 0, v[146:147]
	s_mov_b32 m0, s54
	s_nop 0
	global_load_lds_dwordx4 v[206:207], off
	v_lshl_add_u64 v[206:207], s[0:1], 0, v[150:151]
	s_mov_b32 m0, s55
	s_nop 0
	global_load_lds_dwordx4 v[206:207], off
	v_lshl_add_u64 v[206:207], s[52:53], 0, v[144:145]
	s_mov_b32 m0, s56
	s_nop 0
	global_load_lds_dwordx4 v[206:207], off
	v_lshl_add_u64 v[206:207], s[52:53], 0, v[148:149]
	s_mov_b32 m0, s57
	s_nop 0
	global_load_lds_dwordx4 v[206:207], off
	s_waitcnt vmcnt(8)
	s_waitcnt lgkmcnt(0)
	s_setprio 1
	s_barrier
	v_mfma_f32_16x16x32_bf16 v[60:63], v[108:111], v[174:177], 0
	v_mfma_f32_16x16x32_bf16 v[56:59], v[120:123], v[174:177], 0
	v_mfma_f32_16x16x32_bf16 v[44:47], v[108:111], v[182:185], 0
	v_mfma_f32_16x16x32_bf16 v[40:43], v[120:123], v[182:185], 0
	v_mfma_f32_16x16x32_bf16 v[28:31], v[108:111], v[190:193], 0
	v_mfma_f32_16x16x32_bf16 v[24:27], v[120:123], v[190:193], 0
	v_mfma_f32_16x16x32_bf16 v[12:15], v[108:111], v[198:201], 0
	v_mfma_f32_16x16x32_bf16 v[8:11], v[120:123], v[198:201], 0
	v_mfma_f32_16x16x32_bf16 v[60:63], v[112:115], v[178:181], v[60:63]
	v_mfma_f32_16x16x32_bf16 v[56:59], v[124:127], v[178:181], v[56:59]
	v_mfma_f32_16x16x32_bf16 v[44:47], v[112:115], v[186:189], v[44:47]
	v_mfma_f32_16x16x32_bf16 v[40:43], v[124:127], v[186:189], v[40:43]
	v_mfma_f32_16x16x32_bf16 v[28:31], v[112:115], v[194:197], v[28:31]
	v_mfma_f32_16x16x32_bf16 v[24:27], v[124:127], v[194:197], v[24:27]
	v_mfma_f32_16x16x32_bf16 v[12:15], v[112:115], v[202:205], v[12:15]
	v_mfma_f32_16x16x32_bf16 v[8:11], v[124:127], v[202:205], v[8:11]
	s_setprio 0
	s_setprio 1
	v_mfma_f32_16x16x32_bf16 v[52:55], v[158:161], v[174:177], 0
	v_mfma_f32_16x16x32_bf16 v[48:51], v[166:169], v[174:177], 0
	v_mfma_f32_16x16x32_bf16 v[36:39], v[158:161], v[182:185], 0
	v_mfma_f32_16x16x32_bf16 v[32:35], v[166:169], v[182:185], 0
	v_mfma_f32_16x16x32_bf16 v[20:23], v[158:161], v[190:193], 0
	v_mfma_f32_16x16x32_bf16 v[16:19], v[166:169], v[190:193], 0
	v_mfma_f32_16x16x32_bf16 v[4:7], v[158:161], v[198:201], 0
	v_mfma_f32_16x16x32_bf16 v[0:3], v[166:169], v[198:201], 0
	v_mfma_f32_16x16x32_bf16 v[52:55], v[162:165], v[178:181], v[52:55]
	v_mfma_f32_16x16x32_bf16 v[48:51], v[170:173], v[178:181], v[48:51]
	v_mfma_f32_16x16x32_bf16 v[36:39], v[162:165], v[186:189], v[36:39]
	v_mfma_f32_16x16x32_bf16 v[32:35], v[170:173], v[186:189], v[32:35]
	v_mfma_f32_16x16x32_bf16 v[20:23], v[162:165], v[194:197], v[20:23]
	v_mfma_f32_16x16x32_bf16 v[16:19], v[170:173], v[194:197], v[16:19]
	v_mfma_f32_16x16x32_bf16 v[4:7], v[162:165], v[202:205], v[4:7]
	v_mfma_f32_16x16x32_bf16 v[0:3], v[170:173], v[202:205], v[0:3]
	s_barrier
	s_setprio 0
	v_add_u32_e32 v124, s62, v156
	v_add_u32_e32 v170, s67, v156
	ds_read_b128 v[108:111], v124
	ds_read_b128 v[112:115], v124 offset:1024
	ds_read_b128 v[120:123], v124 offset:2048
	ds_read_b128 v[124:127], v124 offset:3072
	ds_read_b128 v[158:161], v170
	ds_read_b128 v[162:165], v170 offset:1024
	ds_read_b128 v[166:169], v170 offset:2048
	ds_read_b128 v[170:173], v170 offset:3072
	ds_read_b128 v[174:177], v157 offset:32768
	ds_read_b128 v[178:181], v157 offset:33792
	ds_read_b128 v[182:185], v157 offset:34816
	ds_read_b128 v[186:189], v157 offset:35840
	ds_read_b128 v[190:193], v157 offset:36864
	ds_read_b128 v[194:197], v157 offset:37888
	ds_read_b128 v[198:201], v157 offset:38912
	ds_read_b128 v[202:205], v157 offset:39936
	s_add_u32 s0, s52, 0x4000
	s_addc_u32 s1, s53, 0
	s_mov_b32 m0, s58
	v_lshl_add_u64 v[206:207], s[0:1], 0, v[144:145]
	global_load_lds_dwordx4 v[206:207], off
	v_lshl_add_u64 v[206:207], s[0:1], 0, v[148:149]
	s_mov_b32 m0, s59
	s_nop 0
	global_load_lds_dwordx4 v[206:207], off
	s_waitcnt vmcnt(8)
	s_waitcnt lgkmcnt(0)
	s_setprio 1
	s_barrier
	v_mfma_f32_16x16x32_bf16 v[140:143], v[108:111], v[174:177], v[140:143]
	v_mfma_f32_16x16x32_bf16 v[136:139], v[120:123], v[174:177], v[136:139]
	v_mfma_f32_16x16x32_bf16 v[116:119], v[108:111], v[182:185], v[116:119]
	v_mfma_f32_16x16x32_bf16 v[104:107], v[120:123], v[182:185], v[104:107]
	v_mfma_f32_16x16x32_bf16 v[92:95], v[108:111], v[190:193], v[92:95]
	v_mfma_f32_16x16x32_bf16 v[88:91], v[120:123], v[190:193], v[88:91]
	v_mfma_f32_16x16x32_bf16 v[76:79], v[108:111], v[198:201], v[76:79]
	v_mfma_f32_16x16x32_bf16 v[72:75], v[120:123], v[198:201], v[72:75]
	v_mfma_f32_16x16x32_bf16 v[140:143], v[112:115], v[178:181], v[140:143]
	v_mfma_f32_16x16x32_bf16 v[136:139], v[124:127], v[178:181], v[136:139]
	v_mfma_f32_16x16x32_bf16 v[116:119], v[112:115], v[186:189], v[116:119]
	v_mfma_f32_16x16x32_bf16 v[104:107], v[124:127], v[186:189], v[104:107]
	v_mfma_f32_16x16x32_bf16 v[92:95], v[112:115], v[194:197], v[92:95]
	v_mfma_f32_16x16x32_bf16 v[88:91], v[124:127], v[194:197], v[88:91]
	v_mfma_f32_16x16x32_bf16 v[76:79], v[112:115], v[202:205], v[76:79]
	v_mfma_f32_16x16x32_bf16 v[72:75], v[124:127], v[202:205], v[72:75]
	s_setprio 0
	s_setprio 1
	v_mfma_f32_16x16x32_bf16 v[132:135], v[158:161], v[174:177], v[132:135]
	v_mfma_f32_16x16x32_bf16 v[128:131], v[166:169], v[174:177], v[128:131]
	v_mfma_f32_16x16x32_bf16 v[100:103], v[158:161], v[182:185], v[100:103]
	v_mfma_f32_16x16x32_bf16 v[96:99], v[166:169], v[182:185], v[96:99]
	v_mfma_f32_16x16x32_bf16 v[84:87], v[158:161], v[190:193], v[84:87]
	v_mfma_f32_16x16x32_bf16 v[80:83], v[166:169], v[190:193], v[80:83]
	v_mfma_f32_16x16x32_bf16 v[68:71], v[158:161], v[198:201], v[68:71]
	v_mfma_f32_16x16x32_bf16 v[64:67], v[166:169], v[198:201], v[64:67]
	v_mfma_f32_16x16x32_bf16 v[132:135], v[162:165], v[178:181], v[132:135]
	v_mfma_f32_16x16x32_bf16 v[128:131], v[170:173], v[178:181], v[128:131]
	v_mfma_f32_16x16x32_bf16 v[100:103], v[162:165], v[186:189], v[100:103]
	v_mfma_f32_16x16x32_bf16 v[96:99], v[170:173], v[186:189], v[96:99]
	v_mfma_f32_16x16x32_bf16 v[84:87], v[162:165], v[194:197], v[84:87]
	v_mfma_f32_16x16x32_bf16 v[80:83], v[170:173], v[194:197], v[80:83]
	v_mfma_f32_16x16x32_bf16 v[68:71], v[162:165], v[202:205], v[68:71]
	v_mfma_f32_16x16x32_bf16 v[64:67], v[170:173], v[202:205], v[64:67]
	s_barrier
	s_setprio 0
	ds_read_b128 v[174:177], v157 offset:49152
	ds_read_b128 v[178:181], v157 offset:50176
	ds_read_b128 v[182:185], v157 offset:51200
	ds_read_b128 v[186:189], v157 offset:52224
	ds_read_b128 v[190:193], v157 offset:53248
	ds_read_b128 v[194:197], v157 offset:54272
	ds_read_b128 v[198:201], v157 offset:55296
	ds_read_b128 v[202:205], v157 offset:56320
	s_add_u32 s0, s50, 0x8000
	s_addc_u32 s1, s51, 0
	s_mov_b32 m0, s63
	v_lshl_add_u64 v[206:207], s[0:1], 0, v[146:147]
	global_load_lds_dwordx4 v[206:207], off
	v_lshl_add_u64 v[206:207], s[0:1], 0, v[150:151]
	s_add_u32 s0, s50, 0xc000
	s_mov_b32 m0, s64
	s_addc_u32 s1, s51, 0
	global_load_lds_dwordx4 v[206:207], off
	v_lshl_add_u64 v[206:207], s[0:1], 0, v[146:147]
	s_mov_b32 m0, s68
	s_nop 0
	global_load_lds_dwordx4 v[206:207], off
	v_lshl_add_u64 v[206:207], s[0:1], 0, v[150:151]
	s_mov_b32 m0, s69
	s_nop 0
	global_load_lds_dwordx4 v[206:207], off
	v_lshl_add_u64 v[206:207], s[48:49], 0, v[144:145]
	s_mov_b32 m0, s65
	s_nop 0
	global_load_lds_dwordx4 v[206:207], off
	v_lshl_add_u64 v[206:207], s[48:49], 0, v[148:149]
	s_mov_b32 m0, s66
	s_nop 0
	global_load_lds_dwordx4 v[206:207], off
	s_waitcnt vmcnt(8)
	s_waitcnt lgkmcnt(0)
	s_setprio 1
	s_barrier
	v_mfma_f32_16x16x32_bf16 v[60:63], v[108:111], v[174:177], v[60:63]
	v_mfma_f32_16x16x32_bf16 v[56:59], v[120:123], v[174:177], v[56:59]
	v_mfma_f32_16x16x32_bf16 v[44:47], v[108:111], v[182:185], v[44:47]
	v_mfma_f32_16x16x32_bf16 v[40:43], v[120:123], v[182:185], v[40:43]
	v_mfma_f32_16x16x32_bf16 v[28:31], v[108:111], v[190:193], v[28:31]
	v_mfma_f32_16x16x32_bf16 v[24:27], v[120:123], v[190:193], v[24:27]
	v_mfma_f32_16x16x32_bf16 v[12:15], v[108:111], v[198:201], v[12:15]
	v_mfma_f32_16x16x32_bf16 v[8:11], v[120:123], v[198:201], v[8:11]
	v_mfma_f32_16x16x32_bf16 v[60:63], v[112:115], v[178:181], v[60:63]
	v_mfma_f32_16x16x32_bf16 v[56:59], v[124:127], v[178:181], v[56:59]
	v_mfma_f32_16x16x32_bf16 v[44:47], v[112:115], v[186:189], v[44:47]
	v_mfma_f32_16x16x32_bf16 v[40:43], v[124:127], v[186:189], v[40:43]
	v_mfma_f32_16x16x32_bf16 v[28:31], v[112:115], v[194:197], v[28:31]
	v_mfma_f32_16x16x32_bf16 v[24:27], v[124:127], v[194:197], v[24:27]
	v_mfma_f32_16x16x32_bf16 v[12:15], v[112:115], v[202:205], v[12:15]
	v_mfma_f32_16x16x32_bf16 v[8:11], v[124:127], v[202:205], v[8:11]
	s_setprio 0
	s_setprio 1
	v_mfma_f32_16x16x32_bf16 v[52:55], v[158:161], v[174:177], v[52:55]
	v_mfma_f32_16x16x32_bf16 v[48:51], v[166:169], v[174:177], v[48:51]
	v_mfma_f32_16x16x32_bf16 v[36:39], v[158:161], v[182:185], v[36:39]
	v_mfma_f32_16x16x32_bf16 v[32:35], v[166:169], v[182:185], v[32:35]
	v_mfma_f32_16x16x32_bf16 v[20:23], v[158:161], v[190:193], v[20:23]
	v_mfma_f32_16x16x32_bf16 v[16:19], v[166:169], v[190:193], v[16:19]
	v_mfma_f32_16x16x32_bf16 v[4:7], v[158:161], v[198:201], v[4:7]
	v_mfma_f32_16x16x32_bf16 v[0:3], v[166:169], v[198:201], v[0:3]
	v_mfma_f32_16x16x32_bf16 v[52:55], v[162:165], v[178:181], v[52:55]
	v_mfma_f32_16x16x32_bf16 v[48:51], v[170:173], v[178:181], v[48:51]
	v_mfma_f32_16x16x32_bf16 v[36:39], v[162:165], v[186:189], v[36:39]
	v_mfma_f32_16x16x32_bf16 v[32:35], v[170:173], v[186:189], v[32:35]
	v_mfma_f32_16x16x32_bf16 v[20:23], v[162:165], v[194:197], v[20:23]
	v_mfma_f32_16x16x32_bf16 v[16:19], v[170:173], v[194:197], v[16:19]
	v_mfma_f32_16x16x32_bf16 v[4:7], v[162:165], v[202:205], v[4:7]
	v_mfma_f32_16x16x32_bf16 v[0:3], v[170:173], v[202:205], v[0:3]
	s_barrier
	s_setprio 0
	s_add_i32 s78, s78, 2
	s_add_u32 s76, s76, 0x10000
	s_addc_u32 s77, s77, 0
	s_cmp_gt_u32 s78, 29
	s_mov_b64 s[0:1], s[46:47]
.LBB0_1173:
	v_add_u32_e32 v124, s28, v156
	v_add_u32_e32 v170, s45, v156
	ds_read_b128 v[108:111], v124
	ds_read_b128 v[112:115], v124 offset:1024
	ds_read_b128 v[120:123], v124 offset:2048
	ds_read_b128 v[124:127], v124 offset:3072
	ds_read_b128 v[158:161], v170
	ds_read_b128 v[162:165], v170 offset:1024
	ds_read_b128 v[166:169], v170 offset:2048
	ds_read_b128 v[170:173], v170 offset:3072
	ds_read_b128 v[174:177], v157
	ds_read_b128 v[178:181], v157 offset:1024
	ds_read_b128 v[182:185], v157 offset:2048
	ds_read_b128 v[186:189], v157 offset:3072
	ds_read_b128 v[190:193], v157 offset:4096
	ds_read_b128 v[194:197], v157 offset:5120
	ds_read_b128 v[198:201], v157 offset:6144
	ds_read_b128 v[202:205], v157 offset:7168
	s_add_u32 s46, s0, 0x10000
	s_addc_u32 s47, s1, 0
	s_cmp_eq_u32 s78, 28
	s_cselect_b32 s52, s5, s46
	s_cselect_b32 s53, s4, s47
	s_cselect_b32 s50, s39, s76
	s_cselect_b32 s51, s35, s77
	s_add_u32 s48, s52, 0x8000
	s_addc_u32 s49, s53, 0
	v_lshl_add_u64 v[206:207], s[0:1], 0, v[152:153]
	s_add_i32 m0, s56, 0xc000
	s_nop 0
	global_load_lds_dwordx4 v[206:207], off
	v_lshl_add_u64 v[206:207], s[0:1], 0, v[154:155]
	s_add_i32 m0, s56, 0xe000
	s_nop 0
	global_load_lds_dwordx4 v[206:207], off
	s_waitcnt vmcnt(8)
	s_waitcnt lgkmcnt(0)
	s_setprio 1
	s_barrier
	v_mfma_f32_16x16x32_bf16 v[140:143], v[108:111], v[174:177], v[140:143]
	v_mfma_f32_16x16x32_bf16 v[136:139], v[120:123], v[174:177], v[136:139]
	v_mfma_f32_16x16x32_bf16 v[116:119], v[108:111], v[182:185], v[116:119]
	v_mfma_f32_16x16x32_bf16 v[104:107], v[120:123], v[182:185], v[104:107]
	v_mfma_f32_16x16x32_bf16 v[92:95], v[108:111], v[190:193], v[92:95]
	v_mfma_f32_16x16x32_bf16 v[88:91], v[120:123], v[190:193], v[88:91]
	v_mfma_f32_16x16x32_bf16 v[76:79], v[108:111], v[198:201], v[76:79]
	v_mfma_f32_16x16x32_bf16 v[72:75], v[120:123], v[198:201], v[72:75]
	v_mfma_f32_16x16x32_bf16 v[140:143], v[112:115], v[178:181], v[140:143]
	v_mfma_f32_16x16x32_bf16 v[136:139], v[124:127], v[178:181], v[136:139]
	v_mfma_f32_16x16x32_bf16 v[116:119], v[112:115], v[186:189], v[116:119]
	v_mfma_f32_16x16x32_bf16 v[104:107], v[124:127], v[186:189], v[104:107]
	v_mfma_f32_16x16x32_bf16 v[92:95], v[112:115], v[194:197], v[92:95]
	v_mfma_f32_16x16x32_bf16 v[88:91], v[124:127], v[194:197], v[88:91]
	v_mfma_f32_16x16x32_bf16 v[76:79], v[112:115], v[202:205], v[76:79]
	v_mfma_f32_16x16x32_bf16 v[72:75], v[124:127], v[202:205], v[72:75]
	s_setprio 0
	s_setprio 1
	v_mfma_f32_16x16x32_bf16 v[132:135], v[158:161], v[174:177], v[132:135]
	v_mfma_f32_16x16x32_bf16 v[128:131], v[166:169], v[174:177], v[128:131]
	v_mfma_f32_16x16x32_bf16 v[100:103], v[158:161], v[182:185], v[100:103]
	v_mfma_f32_16x16x32_bf16 v[96:99], v[166:169], v[182:185], v[96:99]
	v_mfma_f32_16x16x32_bf16 v[84:87], v[158:161], v[190:193], v[84:87]
	v_mfma_f32_16x16x32_bf16 v[80:83], v[166:169], v[190:193], v[80:83]
	v_mfma_f32_16x16x32_bf16 v[68:71], v[158:161], v[198:201], v[68:71]
	v_mfma_f32_16x16x32_bf16 v[64:67], v[166:169], v[198:201], v[64:67]
	v_mfma_f32_16x16x32_bf16 v[132:135], v[162:165], v[178:181], v[132:135]
	v_mfma_f32_16x16x32_bf16 v[128:131], v[170:173], v[178:181], v[128:131]
	v_mfma_f32_16x16x32_bf16 v[100:103], v[162:165], v[186:189], v[100:103]
	v_mfma_f32_16x16x32_bf16 v[96:99], v[170:173], v[186:189], v[96:99]
	v_mfma_f32_16x16x32_bf16 v[84:87], v[162:165], v[194:197], v[84:87]
	v_mfma_f32_16x16x32_bf16 v[80:83], v[170:173], v[194:197], v[80:83]
	v_mfma_f32_16x16x32_bf16 v[68:71], v[162:165], v[202:205], v[68:71]
	v_mfma_f32_16x16x32_bf16 v[64:67], v[170:173], v[202:205], v[64:67]
	s_barrier
	s_setprio 0
	ds_read_b128 v[174:177], v157 offset:16384
	ds_read_b128 v[178:181], v157 offset:17408
	ds_read_b128 v[182:185], v157 offset:18432
	ds_read_b128 v[186:189], v157 offset:19456
	ds_read_b128 v[190:193], v157 offset:20480
	ds_read_b128 v[194:197], v157 offset:21504
	ds_read_b128 v[198:201], v157 offset:22528
	ds_read_b128 v[202:205], v157 offset:23552
	s_mov_b32 m0, s30
	v_lshl_add_u64 v[206:207], s[50:51], 0, v[146:147]
	s_add_u32 s0, s50, 0x4000
	global_load_lds_dwordx4 v[206:207], off
	v_lshl_add_u64 v[206:207], s[50:51], 0, v[150:151]
	s_mov_b32 m0, s31
	s_addc_u32 s1, s51, 0
	global_load_lds_dwordx4 v[206:207], off
	v_lshl_add_u64 v[206:207], s[0:1], 0, v[146:147]
	s_mov_b32 m0, s54
	s_nop 0
	global_load_lds_dwordx4 v[206:207], off
	v_lshl_add_u64 v[206:207], s[0:1], 0, v[150:151]
	s_mov_b32 m0, s55
	s_nop 0
	global_load_lds_dwordx4 v[206:207], off
	v_lshl_add_u64 v[206:207], s[52:53], 0, v[144:145]
	s_mov_b32 m0, s56
	s_nop 0
	global_load_lds_dwordx4 v[206:207], off
	v_lshl_add_u64 v[206:207], s[52:53], 0, v[148:149]
	s_mov_b32 m0, s57
	s_nop 0
	global_load_lds_dwordx4 v[206:207], off
	s_waitcnt vmcnt(8)
	s_waitcnt lgkmcnt(0)
	s_setprio 1
	s_barrier
	v_mfma_f32_16x16x32_bf16 v[60:63], v[108:111], v[174:177], v[60:63]
	v_mfma_f32_16x16x32_bf16 v[56:59], v[120:123], v[174:177], v[56:59]
	v_mfma_f32_16x16x32_bf16 v[44:47], v[108:111], v[182:185], v[44:47]
	v_mfma_f32_16x16x32_bf16 v[40:43], v[120:123], v[182:185], v[40:43]
	v_mfma_f32_16x16x32_bf16 v[28:31], v[108:111], v[190:193], v[28:31]
	v_mfma_f32_16x16x32_bf16 v[24:27], v[120:123], v[190:193], v[24:27]
	v_mfma_f32_16x16x32_bf16 v[12:15], v[108:111], v[198:201], v[12:15]
	v_mfma_f32_16x16x32_bf16 v[8:11], v[120:123], v[198:201], v[8:11]
	v_mfma_f32_16x16x32_bf16 v[60:63], v[112:115], v[178:181], v[60:63]
	v_mfma_f32_16x16x32_bf16 v[56:59], v[124:127], v[178:181], v[56:59]
	v_mfma_f32_16x16x32_bf16 v[44:47], v[112:115], v[186:189], v[44:47]
	v_mfma_f32_16x16x32_bf16 v[40:43], v[124:127], v[186:189], v[40:43]
	v_mfma_f32_16x16x32_bf16 v[28:31], v[112:115], v[194:197], v[28:31]
	v_mfma_f32_16x16x32_bf16 v[24:27], v[124:127], v[194:197], v[24:27]
	v_mfma_f32_16x16x32_bf16 v[12:15], v[112:115], v[202:205], v[12:15]
	v_mfma_f32_16x16x32_bf16 v[8:11], v[124:127], v[202:205], v[8:11]
	s_setprio 0
	s_setprio 1
	v_mfma_f32_16x16x32_bf16 v[52:55], v[158:161], v[174:177], v[52:55]
	v_mfma_f32_16x16x32_bf16 v[48:51], v[166:169], v[174:177], v[48:51]
	v_mfma_f32_16x16x32_bf16 v[36:39], v[158:161], v[182:185], v[36:39]
	v_mfma_f32_16x16x32_bf16 v[32:35], v[166:169], v[182:185], v[32:35]
	v_mfma_f32_16x16x32_bf16 v[20:23], v[158:161], v[190:193], v[20:23]
	v_mfma_f32_16x16x32_bf16 v[16:19], v[166:169], v[190:193], v[16:19]
	v_mfma_f32_16x16x32_bf16 v[4:7], v[158:161], v[198:201], v[4:7]
	v_mfma_f32_16x16x32_bf16 v[0:3], v[166:169], v[198:201], v[0:3]
	v_mfma_f32_16x16x32_bf16 v[52:55], v[162:165], v[178:181], v[52:55]
	v_mfma_f32_16x16x32_bf16 v[48:51], v[170:173], v[178:181], v[48:51]
	v_mfma_f32_16x16x32_bf16 v[36:39], v[162:165], v[186:189], v[36:39]
	v_mfma_f32_16x16x32_bf16 v[32:35], v[170:173], v[186:189], v[32:35]
	v_mfma_f32_16x16x32_bf16 v[20:23], v[162:165], v[194:197], v[20:23]
	v_mfma_f32_16x16x32_bf16 v[16:19], v[170:173], v[194:197], v[16:19]
	v_mfma_f32_16x16x32_bf16 v[4:7], v[162:165], v[202:205], v[4:7]
	v_mfma_f32_16x16x32_bf16 v[0:3], v[170:173], v[202:205], v[0:3]
	s_barrier
	s_setprio 0
	v_add_u32_e32 v124, s62, v156
	v_add_u32_e32 v170, s67, v156
	ds_read_b128 v[108:111], v124
	ds_read_b128 v[112:115], v124 offset:1024
	ds_read_b128 v[120:123], v124 offset:2048
	ds_read_b128 v[124:127], v124 offset:3072
	ds_read_b128 v[158:161], v170
	ds_read_b128 v[162:165], v170 offset:1024
	ds_read_b128 v[166:169], v170 offset:2048
	ds_read_b128 v[170:173], v170 offset:3072
	ds_read_b128 v[174:177], v157 offset:32768
	ds_read_b128 v[178:181], v157 offset:33792
	ds_read_b128 v[182:185], v157 offset:34816
	ds_read_b128 v[186:189], v157 offset:35840
	ds_read_b128 v[190:193], v157 offset:36864
	ds_read_b128 v[194:197], v157 offset:37888
	ds_read_b128 v[198:201], v157 offset:38912
	ds_read_b128 v[202:205], v157 offset:39936
	s_add_u32 s0, s52, 0x4000
	s_addc_u32 s1, s53, 0
	s_mov_b32 m0, s58
	v_lshl_add_u64 v[206:207], s[0:1], 0, v[144:145]
	global_load_lds_dwordx4 v[206:207], off
	v_lshl_add_u64 v[206:207], s[0:1], 0, v[148:149]
	s_mov_b32 m0, s59
	s_nop 0
	global_load_lds_dwordx4 v[206:207], off
	s_waitcnt vmcnt(8)
	s_waitcnt lgkmcnt(0)
	s_setprio 1
	s_barrier
	v_mfma_f32_16x16x32_bf16 v[140:143], v[108:111], v[174:177], v[140:143]
	v_mfma_f32_16x16x32_bf16 v[136:139], v[120:123], v[174:177], v[136:139]
	v_mfma_f32_16x16x32_bf16 v[116:119], v[108:111], v[182:185], v[116:119]
	v_mfma_f32_16x16x32_bf16 v[104:107], v[120:123], v[182:185], v[104:107]
	v_mfma_f32_16x16x32_bf16 v[92:95], v[108:111], v[190:193], v[92:95]
	v_mfma_f32_16x16x32_bf16 v[88:91], v[120:123], v[190:193], v[88:91]
	v_mfma_f32_16x16x32_bf16 v[76:79], v[108:111], v[198:201], v[76:79]
	v_mfma_f32_16x16x32_bf16 v[72:75], v[120:123], v[198:201], v[72:75]
	v_mfma_f32_16x16x32_bf16 v[140:143], v[112:115], v[178:181], v[140:143]
	v_mfma_f32_16x16x32_bf16 v[136:139], v[124:127], v[178:181], v[136:139]
	v_mfma_f32_16x16x32_bf16 v[116:119], v[112:115], v[186:189], v[116:119]
	v_mfma_f32_16x16x32_bf16 v[104:107], v[124:127], v[186:189], v[104:107]
	v_mfma_f32_16x16x32_bf16 v[92:95], v[112:115], v[194:197], v[92:95]
	v_mfma_f32_16x16x32_bf16 v[88:91], v[124:127], v[194:197], v[88:91]
	v_mfma_f32_16x16x32_bf16 v[76:79], v[112:115], v[202:205], v[76:79]
	v_mfma_f32_16x16x32_bf16 v[72:75], v[124:127], v[202:205], v[72:75]
	s_setprio 0
	s_setprio 1
	v_mfma_f32_16x16x32_bf16 v[132:135], v[158:161], v[174:177], v[132:135]
	v_mfma_f32_16x16x32_bf16 v[128:131], v[166:169], v[174:177], v[128:131]
	v_mfma_f32_16x16x32_bf16 v[100:103], v[158:161], v[182:185], v[100:103]
	v_mfma_f32_16x16x32_bf16 v[96:99], v[166:169], v[182:185], v[96:99]
	v_mfma_f32_16x16x32_bf16 v[84:87], v[158:161], v[190:193], v[84:87]
	v_mfma_f32_16x16x32_bf16 v[80:83], v[166:169], v[190:193], v[80:83]
	v_mfma_f32_16x16x32_bf16 v[68:71], v[158:161], v[198:201], v[68:71]
	v_mfma_f32_16x16x32_bf16 v[64:67], v[166:169], v[198:201], v[64:67]
	v_mfma_f32_16x16x32_bf16 v[132:135], v[162:165], v[178:181], v[132:135]
	v_mfma_f32_16x16x32_bf16 v[128:131], v[170:173], v[178:181], v[128:131]
	v_mfma_f32_16x16x32_bf16 v[100:103], v[162:165], v[186:189], v[100:103]
	v_mfma_f32_16x16x32_bf16 v[96:99], v[170:173], v[186:189], v[96:99]
	v_mfma_f32_16x16x32_bf16 v[84:87], v[162:165], v[194:197], v[84:87]
	v_mfma_f32_16x16x32_bf16 v[80:83], v[170:173], v[194:197], v[80:83]
	v_mfma_f32_16x16x32_bf16 v[68:71], v[162:165], v[202:205], v[68:71]
	v_mfma_f32_16x16x32_bf16 v[64:67], v[170:173], v[202:205], v[64:67]
	s_barrier
	s_setprio 0
	ds_read_b128 v[174:177], v157 offset:49152
	ds_read_b128 v[178:181], v157 offset:50176
	ds_read_b128 v[182:185], v157 offset:51200
	ds_read_b128 v[186:189], v157 offset:52224
	ds_read_b128 v[190:193], v157 offset:53248
	ds_read_b128 v[194:197], v157 offset:54272
	ds_read_b128 v[198:201], v157 offset:55296
	ds_read_b128 v[202:205], v157 offset:56320
	s_add_u32 s0, s50, 0x8000
	s_addc_u32 s1, s51, 0
	s_mov_b32 m0, s63
	v_lshl_add_u64 v[206:207], s[0:1], 0, v[146:147]
	global_load_lds_dwordx4 v[206:207], off
	v_lshl_add_u64 v[206:207], s[0:1], 0, v[150:151]
	s_add_u32 s0, s50, 0xc000
	s_mov_b32 m0, s64
	s_addc_u32 s1, s51, 0
	global_load_lds_dwordx4 v[206:207], off
	v_lshl_add_u64 v[206:207], s[0:1], 0, v[146:147]
	s_mov_b32 m0, s68
	s_nop 0
	global_load_lds_dwordx4 v[206:207], off
	v_lshl_add_u64 v[206:207], s[0:1], 0, v[150:151]
	s_mov_b32 m0, s69
	s_nop 0
	global_load_lds_dwordx4 v[206:207], off
	v_lshl_add_u64 v[206:207], s[48:49], 0, v[144:145]
	s_mov_b32 m0, s65
	s_nop 0
	global_load_lds_dwordx4 v[206:207], off
	v_lshl_add_u64 v[206:207], s[48:49], 0, v[148:149]
	s_mov_b32 m0, s66
	s_nop 0
	global_load_lds_dwordx4 v[206:207], off
	s_waitcnt vmcnt(8)
	s_waitcnt lgkmcnt(0)
	s_setprio 1
	s_barrier
	v_mfma_f32_16x16x32_bf16 v[60:63], v[108:111], v[174:177], v[60:63]
	v_mfma_f32_16x16x32_bf16 v[56:59], v[120:123], v[174:177], v[56:59]
	v_mfma_f32_16x16x32_bf16 v[44:47], v[108:111], v[182:185], v[44:47]
	v_mfma_f32_16x16x32_bf16 v[40:43], v[120:123], v[182:185], v[40:43]
	v_mfma_f32_16x16x32_bf16 v[28:31], v[108:111], v[190:193], v[28:31]
	v_mfma_f32_16x16x32_bf16 v[24:27], v[120:123], v[190:193], v[24:27]
	v_mfma_f32_16x16x32_bf16 v[12:15], v[108:111], v[198:201], v[12:15]
	v_mfma_f32_16x16x32_bf16 v[8:11], v[120:123], v[198:201], v[8:11]
	v_mfma_f32_16x16x32_bf16 v[60:63], v[112:115], v[178:181], v[60:63]
	v_mfma_f32_16x16x32_bf16 v[56:59], v[124:127], v[178:181], v[56:59]
	v_mfma_f32_16x16x32_bf16 v[44:47], v[112:115], v[186:189], v[44:47]
	v_mfma_f32_16x16x32_bf16 v[40:43], v[124:127], v[186:189], v[40:43]
	v_mfma_f32_16x16x32_bf16 v[28:31], v[112:115], v[194:197], v[28:31]
	v_mfma_f32_16x16x32_bf16 v[24:27], v[124:127], v[194:197], v[24:27]
	v_mfma_f32_16x16x32_bf16 v[12:15], v[112:115], v[202:205], v[12:15]
	v_mfma_f32_16x16x32_bf16 v[8:11], v[124:127], v[202:205], v[8:11]
	s_setprio 0
	s_setprio 1
	v_mfma_f32_16x16x32_bf16 v[52:55], v[158:161], v[174:177], v[52:55]
	v_mfma_f32_16x16x32_bf16 v[48:51], v[166:169], v[174:177], v[48:51]
	v_mfma_f32_16x16x32_bf16 v[36:39], v[158:161], v[182:185], v[36:39]
	v_mfma_f32_16x16x32_bf16 v[32:35], v[166:169], v[182:185], v[32:35]
	v_mfma_f32_16x16x32_bf16 v[20:23], v[158:161], v[190:193], v[20:23]
	v_mfma_f32_16x16x32_bf16 v[16:19], v[166:169], v[190:193], v[16:19]
	v_mfma_f32_16x16x32_bf16 v[4:7], v[158:161], v[198:201], v[4:7]
	v_mfma_f32_16x16x32_bf16 v[0:3], v[166:169], v[198:201], v[0:3]
	v_mfma_f32_16x16x32_bf16 v[52:55], v[162:165], v[178:181], v[52:55]
	v_mfma_f32_16x16x32_bf16 v[48:51], v[170:173], v[178:181], v[48:51]
	v_mfma_f32_16x16x32_bf16 v[36:39], v[162:165], v[186:189], v[36:39]
	v_mfma_f32_16x16x32_bf16 v[32:35], v[170:173], v[186:189], v[32:35]
	v_mfma_f32_16x16x32_bf16 v[20:23], v[162:165], v[194:197], v[20:23]
	v_mfma_f32_16x16x32_bf16 v[16:19], v[170:173], v[194:197], v[16:19]
	v_mfma_f32_16x16x32_bf16 v[4:7], v[162:165], v[202:205], v[4:7]
	v_mfma_f32_16x16x32_bf16 v[0:3], v[170:173], v[202:205], v[0:3]
	s_barrier
	s_setprio 0
	s_add_i32 s78, s78, 2
	s_add_u32 s76, s76, 0x10000
	s_addc_u32 s77, s77, 0
	s_cmp_gt_u32 s78, 29
	s_mov_b64 s[0:1], s[46:47]
	s_cbranch_scc0 .LBB0_1173
	s_and_b64 vcc, exec, s[24:25]
	s_cbranch_vccz .LBB0_1176
	s_barrier

.LBB0_1247:
	s_ashr_i32 s35, s34, 31
	s_lshl_b64 s[4:5], s[34:35], 22
	s_add_u32 s38, s17, s4
	s_addc_u32 s39, s18, s5
	s_and_b64 s[4:5], s[36:37], exec
	s_cselect_b32 s4, s39, s1
	s_cselect_b32 s5, s38, s0
	s_ashr_i32 s25, s24, 31
	s_lshl_b64 s[40:41], s[24:25], 22
	s_add_u32 s40, s19, s40
	s_addc_u32 s41, s28, s41
	s_and_b64 s[46:47], s[36:37], exec
	s_cselect_b32 s25, s41, s45
	s_cselect_b32 s35, s40, s44
	s_add_u32 s74, s44, 0x10000
	s_addc_u32 s75, s45, 0
	s_mov_b32 s76, -2
	v_add_u32_e32 v92, s30, v206
	v_add_u32_e32 v156, s52, v206
	ds_read_b128 v[72:75], v92
	ds_read_b128 v[76:79], v92 offset:1024
	ds_read_b128 v[84:87], v92 offset:2048
	ds_read_b128 v[92:95], v92 offset:3072
	ds_read_b128 v[144:147], v156
	ds_read_b128 v[148:151], v156 offset:1024
	ds_read_b128 v[152:155], v156 offset:2048
	ds_read_b128 v[156:159], v156 offset:3072
	ds_read_b128 v[160:163], v207
	ds_read_b128 v[164:167], v207 offset:1024
	ds_read_b128 v[168:171], v207 offset:2048
	ds_read_b128 v[184:187], v207 offset:3072
	ds_read_b128 v[188:191], v207 offset:4096
	ds_read_b128 v[192:195], v207 offset:5120
	ds_read_b128 v[196:199], v207 offset:6144
	ds_read_b128 v[200:203], v207 offset:7168
	s_add_u32 s44, s0, 0x10000
	s_addc_u32 s45, s1, 0
	s_cmpk_eq_i32 s76, 0x7c
	s_cselect_b32 s50, s5, s44
	s_cselect_b32 s51, s4, s45
	s_cselect_b32 s48, s35, s74
	s_cselect_b32 s49, s25, s75
	s_add_u32 s46, s50, 0x8000
	s_addc_u32 s47, s51, 0
	v_lshl_add_u64 v[204:205], s[0:1], 0, v[180:181]
	s_add_i32 m0, s56, 0xc000
	s_nop 0
	global_load_lds_dwordx4 v[204:205], off
	v_lshl_add_u64 v[204:205], s[0:1], 0, v[182:183]
	s_add_i32 m0, s56, 0xe000
	s_nop 0
	global_load_lds_dwordx4 v[204:205], off
	s_waitcnt vmcnt(8)
	s_waitcnt lgkmcnt(0)
	s_setprio 1
	s_barrier
	v_mfma_f32_16x16x32_bf16 v[140:143], v[72:75], v[160:163], 0
	v_mfma_f32_16x16x32_bf16 v[136:139], v[84:87], v[160:163], 0
	v_mfma_f32_16x16x32_bf16 v[124:127], v[72:75], v[168:171], 0
	v_mfma_f32_16x16x32_bf16 v[120:123], v[84:87], v[168:171], 0
	v_mfma_f32_16x16x32_bf16 v[108:111], v[72:75], v[188:191], 0
	v_mfma_f32_16x16x32_bf16 v[104:107], v[84:87], v[188:191], 0
	v_mfma_f32_16x16x32_bf16 v[88:91], v[72:75], v[196:199], 0
	v_mfma_f32_16x16x32_bf16 v[80:83], v[84:87], v[196:199], 0
	v_mfma_f32_16x16x32_bf16 v[140:143], v[76:79], v[164:167], v[140:143]
	v_mfma_f32_16x16x32_bf16 v[136:139], v[92:95], v[164:167], v[136:139]
	v_mfma_f32_16x16x32_bf16 v[124:127], v[76:79], v[184:187], v[124:127]
	v_mfma_f32_16x16x32_bf16 v[120:123], v[92:95], v[184:187], v[120:123]
	v_mfma_f32_16x16x32_bf16 v[108:111], v[76:79], v[192:195], v[108:111]
	v_mfma_f32_16x16x32_bf16 v[104:107], v[92:95], v[192:195], v[104:107]
	v_mfma_f32_16x16x32_bf16 v[88:91], v[76:79], v[200:203], v[88:91]
	v_mfma_f32_16x16x32_bf16 v[80:83], v[92:95], v[200:203], v[80:83]
	s_setprio 0
	s_setprio 1
	v_mfma_f32_16x16x32_bf16 v[132:135], v[144:147], v[160:163], 0
	v_mfma_f32_16x16x32_bf16 v[128:131], v[152:155], v[160:163], 0
	v_mfma_f32_16x16x32_bf16 v[116:119], v[144:147], v[168:171], 0
	v_mfma_f32_16x16x32_bf16 v[112:115], v[152:155], v[168:171], 0
	v_mfma_f32_16x16x32_bf16 v[100:103], v[144:147], v[188:191], 0
	v_mfma_f32_16x16x32_bf16 v[96:99], v[152:155], v[188:191], 0
	v_mfma_f32_16x16x32_bf16 v[68:71], v[144:147], v[196:199], 0
	v_mfma_f32_16x16x32_bf16 v[64:67], v[152:155], v[196:199], 0
	v_mfma_f32_16x16x32_bf16 v[132:135], v[148:151], v[164:167], v[132:135]
	v_mfma_f32_16x16x32_bf16 v[128:131], v[156:159], v[164:167], v[128:131]
	v_mfma_f32_16x16x32_bf16 v[116:119], v[148:151], v[184:187], v[116:119]
	v_mfma_f32_16x16x32_bf16 v[112:115], v[156:159], v[184:187], v[112:115]
	v_mfma_f32_16x16x32_bf16 v[100:103], v[148:151], v[192:195], v[100:103]
	v_mfma_f32_16x16x32_bf16 v[96:99], v[156:159], v[192:195], v[96:99]
	v_mfma_f32_16x16x32_bf16 v[68:71], v[148:151], v[200:203], v[68:71]
	v_mfma_f32_16x16x32_bf16 v[64:67], v[156:159], v[200:203], v[64:67]
	s_barrier
	s_setprio 0
	ds_read_b128 v[160:163], v207 offset:16384
	ds_read_b128 v[164:167], v207 offset:17408
	ds_read_b128 v[168:171], v207 offset:18432
	ds_read_b128 v[184:187], v207 offset:19456
	ds_read_b128 v[188:191], v207 offset:20480
	ds_read_b128 v[192:195], v207 offset:21504
	ds_read_b128 v[196:199], v207 offset:22528
	ds_read_b128 v[200:203], v207 offset:23552
	s_mov_b32 m0, s31
	v_lshl_add_u64 v[204:205], s[48:49], 0, v[174:175]
	s_add_u32 s0, s48, 0x4000
	global_load_lds_dwordx4 v[204:205], off
	v_lshl_add_u64 v[204:205], s[48:49], 0, v[178:179]
	s_mov_b32 m0, s43
	s_addc_u32 s1, s49, 0
	global_load_lds_dwordx4 v[204:205], off
	v_lshl_add_u64 v[204:205], s[0:1], 0, v[174:175]
	s_mov_b32 m0, s53
	s_nop 0
	global_load_lds_dwordx4 v[204:205], off
	v_lshl_add_u64 v[204:205], s[0:1], 0, v[178:179]
	s_mov_b32 m0, s54
	s_nop 0
	global_load_lds_dwordx4 v[204:205], off
	v_lshl_add_u64 v[204:205], s[50:51], 0, v[172:173]
	s_mov_b32 m0, s56
	s_nop 0
	global_load_lds_dwordx4 v[204:205], off
	v_lshl_add_u64 v[204:205], s[50:51], 0, v[176:177]
	s_mov_b32 m0, s57
	s_nop 0
	global_load_lds_dwordx4 v[204:205], off
	s_waitcnt vmcnt(8)
	s_waitcnt lgkmcnt(0)
	s_setprio 1
	s_barrier
	v_mfma_f32_16x16x32_bf16 v[60:63], v[72:75], v[160:163], 0
	v_mfma_f32_16x16x32_bf16 v[56:59], v[84:87], v[160:163], 0
	v_mfma_f32_16x16x32_bf16 v[44:47], v[72:75], v[168:171], 0
	v_mfma_f32_16x16x32_bf16 v[40:43], v[84:87], v[168:171], 0
	v_mfma_f32_16x16x32_bf16 v[28:31], v[72:75], v[188:191], 0
	v_mfma_f32_16x16x32_bf16 v[24:27], v[84:87], v[188:191], 0
	v_mfma_f32_16x16x32_bf16 v[12:15], v[72:75], v[196:199], 0
	v_mfma_f32_16x16x32_bf16 v[8:11], v[84:87], v[196:199], 0
	v_mfma_f32_16x16x32_bf16 v[60:63], v[76:79], v[164:167], v[60:63]
	v_mfma_f32_16x16x32_bf16 v[56:59], v[92:95], v[164:167], v[56:59]
	v_mfma_f32_16x16x32_bf16 v[44:47], v[76:79], v[184:187], v[44:47]
	v_mfma_f32_16x16x32_bf16 v[40:43], v[92:95], v[184:187], v[40:43]
	v_mfma_f32_16x16x32_bf16 v[28:31], v[76:79], v[192:195], v[28:31]
	v_mfma_f32_16x16x32_bf16 v[24:27], v[92:95], v[192:195], v[24:27]
	v_mfma_f32_16x16x32_bf16 v[12:15], v[76:79], v[200:203], v[12:15]
	v_mfma_f32_16x16x32_bf16 v[8:11], v[92:95], v[200:203], v[8:11]
	s_setprio 0
	s_setprio 1
	v_mfma_f32_16x16x32_bf16 v[52:55], v[144:147], v[160:163], 0
	v_mfma_f32_16x16x32_bf16 v[48:51], v[152:155], v[160:163], 0
	v_mfma_f32_16x16x32_bf16 v[36:39], v[144:147], v[168:171], 0
	v_mfma_f32_16x16x32_bf16 v[32:35], v[152:155], v[168:171], 0
	v_mfma_f32_16x16x32_bf16 v[20:23], v[144:147], v[188:191], 0
	v_mfma_f32_16x16x32_bf16 v[16:19], v[152:155], v[188:191], 0
	v_mfma_f32_16x16x32_bf16 v[4:7], v[144:147], v[196:199], 0
	v_mfma_f32_16x16x32_bf16 v[0:3], v[152:155], v[196:199], 0
	v_mfma_f32_16x16x32_bf16 v[52:55], v[148:151], v[164:167], v[52:55]
	v_mfma_f32_16x16x32_bf16 v[48:51], v[156:159], v[164:167], v[48:51]
	v_mfma_f32_16x16x32_bf16 v[36:39], v[148:151], v[184:187], v[36:39]
	v_mfma_f32_16x16x32_bf16 v[32:35], v[156:159], v[184:187], v[32:35]
	v_mfma_f32_16x16x32_bf16 v[20:23], v[148:151], v[192:195], v[20:23]
	v_mfma_f32_16x16x32_bf16 v[16:19], v[156:159], v[192:195], v[16:19]
	v_mfma_f32_16x16x32_bf16 v[4:7], v[148:151], v[200:203], v[4:7]
	v_mfma_f32_16x16x32_bf16 v[0:3], v[156:159], v[200:203], v[0:3]
	s_barrier
	s_setprio 0
	v_add_u32_e32 v92, s64, v206
	v_add_u32_e32 v156, s69, v206
	ds_read_b128 v[72:75], v92
	ds_read_b128 v[76:79], v92 offset:1024
	ds_read_b128 v[84:87], v92 offset:2048
	ds_read_b128 v[92:95], v92 offset:3072
	ds_read_b128 v[144:147], v156
	ds_read_b128 v[148:151], v156 offset:1024
	ds_read_b128 v[152:155], v156 offset:2048
	ds_read_b128 v[156:159], v156 offset:3072
	ds_read_b128 v[160:163], v207 offset:32768
	ds_read_b128 v[164:167], v207 offset:33792
	ds_read_b128 v[168:171], v207 offset:34816
	ds_read_b128 v[184:187], v207 offset:35840
	ds_read_b128 v[188:191], v207 offset:36864
	ds_read_b128 v[192:195], v207 offset:37888
	ds_read_b128 v[196:199], v207 offset:38912
	ds_read_b128 v[200:203], v207 offset:39936
	s_add_u32 s0, s50, 0x4000
	s_addc_u32 s1, s51, 0
	s_mov_b32 m0, s58
	v_lshl_add_u64 v[204:205], s[0:1], 0, v[172:173]
	global_load_lds_dwordx4 v[204:205], off
	v_lshl_add_u64 v[204:205], s[0:1], 0, v[176:177]
	s_mov_b32 m0, s59
	s_nop 0
	global_load_lds_dwordx4 v[204:205], off
	s_waitcnt vmcnt(8)
	s_waitcnt lgkmcnt(0)
	s_setprio 1
	s_barrier
	v_mfma_f32_16x16x32_bf16 v[140:143], v[72:75], v[160:163], v[140:143]
	v_mfma_f32_16x16x32_bf16 v[136:139], v[84:87], v[160:163], v[136:139]
	v_mfma_f32_16x16x32_bf16 v[124:127], v[72:75], v[168:171], v[124:127]
	v_mfma_f32_16x16x32_bf16 v[120:123], v[84:87], v[168:171], v[120:123]
	v_mfma_f32_16x16x32_bf16 v[108:111], v[72:75], v[188:191], v[108:111]
	v_mfma_f32_16x16x32_bf16 v[104:107], v[84:87], v[188:191], v[104:107]
	v_mfma_f32_16x16x32_bf16 v[88:91], v[72:75], v[196:199], v[88:91]
	v_mfma_f32_16x16x32_bf16 v[80:83], v[84:87], v[196:199], v[80:83]
	v_mfma_f32_16x16x32_bf16 v[140:143], v[76:79], v[164:167], v[140:143]
	v_mfma_f32_16x16x32_bf16 v[136:139], v[92:95], v[164:167], v[136:139]
	v_mfma_f32_16x16x32_bf16 v[124:127], v[76:79], v[184:187], v[124:127]
	v_mfma_f32_16x16x32_bf16 v[120:123], v[92:95], v[184:187], v[120:123]
	v_mfma_f32_16x16x32_bf16 v[108:111], v[76:79], v[192:195], v[108:111]
	v_mfma_f32_16x16x32_bf16 v[104:107], v[92:95], v[192:195], v[104:107]
	v_mfma_f32_16x16x32_bf16 v[88:91], v[76:79], v[200:203], v[88:91]
	v_mfma_f32_16x16x32_bf16 v[80:83], v[92:95], v[200:203], v[80:83]
	s_setprio 0
	s_setprio 1
	v_mfma_f32_16x16x32_bf16 v[132:135], v[144:147], v[160:163], v[132:135]
	v_mfma_f32_16x16x32_bf16 v[128:131], v[152:155], v[160:163], v[128:131]
	v_mfma_f32_16x16x32_bf16 v[116:119], v[144:147], v[168:171], v[116:119]
	v_mfma_f32_16x16x32_bf16 v[112:115], v[152:155], v[168:171], v[112:115]
	v_mfma_f32_16x16x32_bf16 v[100:103], v[144:147], v[188:191], v[100:103]
	v_mfma_f32_16x16x32_bf16 v[96:99], v[152:155], v[188:191], v[96:99]
	v_mfma_f32_16x16x32_bf16 v[68:71], v[144:147], v[196:199], v[68:71]
	v_mfma_f32_16x16x32_bf16 v[64:67], v[152:155], v[196:199], v[64:67]
	v_mfma_f32_16x16x32_bf16 v[132:135], v[148:151], v[164:167], v[132:135]
	v_mfma_f32_16x16x32_bf16 v[128:131], v[156:159], v[164:167], v[128:131]
	v_mfma_f32_16x16x32_bf16 v[116:119], v[148:151], v[184:187], v[116:119]
	v_mfma_f32_16x16x32_bf16 v[112:115], v[156:159], v[184:187], v[112:115]
	v_mfma_f32_16x16x32_bf16 v[100:103], v[148:151], v[192:195], v[100:103]
	v_mfma_f32_16x16x32_bf16 v[96:99], v[156:159], v[192:195], v[96:99]
	v_mfma_f32_16x16x32_bf16 v[68:71], v[148:151], v[200:203], v[68:71]
	v_mfma_f32_16x16x32_bf16 v[64:67], v[156:159], v[200:203], v[64:67]
	s_barrier
	s_setprio 0
	ds_read_b128 v[160:163], v207 offset:49152
	ds_read_b128 v[164:167], v207 offset:50176
	ds_read_b128 v[168:171], v207 offset:51200
	ds_read_b128 v[184:187], v207 offset:52224
	ds_read_b128 v[188:191], v207 offset:53248
	ds_read_b128 v[192:195], v207 offset:54272
	ds_read_b128 v[196:199], v207 offset:55296
	ds_read_b128 v[200:203], v207 offset:56320
	s_add_u32 s0, s48, 0x8000
	s_addc_u32 s1, s49, 0
	s_mov_b32 m0, s65
	v_lshl_add_u64 v[204:205], s[0:1], 0, v[174:175]
	global_load_lds_dwordx4 v[204:205], off
	v_lshl_add_u64 v[204:205], s[0:1], 0, v[178:179]
	s_add_u32 s0, s48, 0xc000
	s_mov_b32 m0, s66
	s_addc_u32 s1, s49, 0
	global_load_lds_dwordx4 v[204:205], off
	v_lshl_add_u64 v[204:205], s[0:1], 0, v[174:175]
	s_mov_b32 m0, s70
	s_nop 0
	global_load_lds_dwordx4 v[204:205], off
	v_lshl_add_u64 v[204:205], s[0:1], 0, v[178:179]
	s_mov_b32 m0, s71
	s_nop 0
	global_load_lds_dwordx4 v[204:205], off
	v_lshl_add_u64 v[204:205], s[46:47], 0, v[172:173]
	s_mov_b32 m0, s67
	s_nop 0
	global_load_lds_dwordx4 v[204:205], off
	v_lshl_add_u64 v[204:205], s[46:47], 0, v[176:177]
	s_mov_b32 m0, s68
	s_nop 0
	global_load_lds_dwordx4 v[204:205], off
	s_waitcnt vmcnt(8)
	s_waitcnt lgkmcnt(0)
	s_setprio 1
	s_barrier
	v_mfma_f32_16x16x32_bf16 v[60:63], v[72:75], v[160:163], v[60:63]
	v_mfma_f32_16x16x32_bf16 v[56:59], v[84:87], v[160:163], v[56:59]
	v_mfma_f32_16x16x32_bf16 v[44:47], v[72:75], v[168:171], v[44:47]
	v_mfma_f32_16x16x32_bf16 v[40:43], v[84:87], v[168:171], v[40:43]
	v_mfma_f32_16x16x32_bf16 v[28:31], v[72:75], v[188:191], v[28:31]
	v_mfma_f32_16x16x32_bf16 v[24:27], v[84:87], v[188:191], v[24:27]
	v_mfma_f32_16x16x32_bf16 v[12:15], v[72:75], v[196:199], v[12:15]
	v_mfma_f32_16x16x32_bf16 v[8:11], v[84:87], v[196:199], v[8:11]
	v_mfma_f32_16x16x32_bf16 v[60:63], v[76:79], v[164:167], v[60:63]
	v_mfma_f32_16x16x32_bf16 v[56:59], v[92:95], v[164:167], v[56:59]
	v_mfma_f32_16x16x32_bf16 v[44:47], v[76:79], v[184:187], v[44:47]
	v_mfma_f32_16x16x32_bf16 v[40:43], v[92:95], v[184:187], v[40:43]
	v_mfma_f32_16x16x32_bf16 v[28:31], v[76:79], v[192:195], v[28:31]
	v_mfma_f32_16x16x32_bf16 v[24:27], v[92:95], v[192:195], v[24:27]
	v_mfma_f32_16x16x32_bf16 v[12:15], v[76:79], v[200:203], v[12:15]
	v_mfma_f32_16x16x32_bf16 v[8:11], v[92:95], v[200:203], v[8:11]
	s_setprio 0
	s_setprio 1
	v_mfma_f32_16x16x32_bf16 v[52:55], v[144:147], v[160:163], v[52:55]
	v_mfma_f32_16x16x32_bf16 v[48:51], v[152:155], v[160:163], v[48:51]
	v_mfma_f32_16x16x32_bf16 v[36:39], v[144:147], v[168:171], v[36:39]
	v_mfma_f32_16x16x32_bf16 v[32:35], v[152:155], v[168:171], v[32:35]
	v_mfma_f32_16x16x32_bf16 v[20:23], v[144:147], v[188:191], v[20:23]
	v_mfma_f32_16x16x32_bf16 v[16:19], v[152:155], v[188:191], v[16:19]
	v_mfma_f32_16x16x32_bf16 v[4:7], v[144:147], v[196:199], v[4:7]
	v_mfma_f32_16x16x32_bf16 v[0:3], v[152:155], v[196:199], v[0:3]
	v_mfma_f32_16x16x32_bf16 v[52:55], v[148:151], v[164:167], v[52:55]
	v_mfma_f32_16x16x32_bf16 v[48:51], v[156:159], v[164:167], v[48:51]
	v_mfma_f32_16x16x32_bf16 v[36:39], v[148:151], v[184:187], v[36:39]
	v_mfma_f32_16x16x32_bf16 v[32:35], v[156:159], v[184:187], v[32:35]
	v_mfma_f32_16x16x32_bf16 v[20:23], v[148:151], v[192:195], v[20:23]
	v_mfma_f32_16x16x32_bf16 v[16:19], v[156:159], v[192:195], v[16:19]
	v_mfma_f32_16x16x32_bf16 v[4:7], v[148:151], v[200:203], v[4:7]
	v_mfma_f32_16x16x32_bf16 v[0:3], v[156:159], v[200:203], v[0:3]
	s_barrier
	s_setprio 0
	s_add_i32 s76, s76, 2
	s_add_u32 s74, s74, 0x10000
	s_addc_u32 s75, s75, 0
	s_cmpk_gt_u32 s76, 0x7d
	s_mov_b64 s[0:1], s[44:45]
.LBB0_1248:
	v_add_u32_e32 v92, s30, v206
	v_add_u32_e32 v156, s52, v206
	ds_read_b128 v[72:75], v92
	ds_read_b128 v[76:79], v92 offset:1024
	ds_read_b128 v[84:87], v92 offset:2048
	ds_read_b128 v[92:95], v92 offset:3072
	ds_read_b128 v[144:147], v156
	ds_read_b128 v[148:151], v156 offset:1024
	ds_read_b128 v[152:155], v156 offset:2048
	ds_read_b128 v[156:159], v156 offset:3072
	ds_read_b128 v[160:163], v207
	ds_read_b128 v[164:167], v207 offset:1024
	ds_read_b128 v[168:171], v207 offset:2048
	ds_read_b128 v[184:187], v207 offset:3072
	ds_read_b128 v[188:191], v207 offset:4096
	ds_read_b128 v[192:195], v207 offset:5120
	ds_read_b128 v[196:199], v207 offset:6144
	ds_read_b128 v[200:203], v207 offset:7168
	s_add_u32 s44, s0, 0x10000
	s_addc_u32 s45, s1, 0
	s_cmpk_eq_i32 s76, 0x7c
	s_cselect_b32 s50, s5, s44
	s_cselect_b32 s51, s4, s45
	s_cselect_b32 s48, s35, s74
	s_cselect_b32 s49, s25, s75
	s_add_u32 s46, s50, 0x8000
	s_addc_u32 s47, s51, 0
	v_lshl_add_u64 v[204:205], s[0:1], 0, v[180:181]
	s_add_i32 m0, s56, 0xc000
	s_nop 0
	global_load_lds_dwordx4 v[204:205], off
	v_lshl_add_u64 v[204:205], s[0:1], 0, v[182:183]
	s_add_i32 m0, s56, 0xe000
	s_nop 0
	global_load_lds_dwordx4 v[204:205], off
	s_waitcnt vmcnt(8)
	s_waitcnt lgkmcnt(0)
	s_setprio 1
	s_barrier
	v_mfma_f32_16x16x32_bf16 v[140:143], v[72:75], v[160:163], v[140:143]
	v_mfma_f32_16x16x32_bf16 v[136:139], v[84:87], v[160:163], v[136:139]
	v_mfma_f32_16x16x32_bf16 v[124:127], v[72:75], v[168:171], v[124:127]
	v_mfma_f32_16x16x32_bf16 v[120:123], v[84:87], v[168:171], v[120:123]
	v_mfma_f32_16x16x32_bf16 v[108:111], v[72:75], v[188:191], v[108:111]
	v_mfma_f32_16x16x32_bf16 v[104:107], v[84:87], v[188:191], v[104:107]
	v_mfma_f32_16x16x32_bf16 v[88:91], v[72:75], v[196:199], v[88:91]
	v_mfma_f32_16x16x32_bf16 v[80:83], v[84:87], v[196:199], v[80:83]
	v_mfma_f32_16x16x32_bf16 v[140:143], v[76:79], v[164:167], v[140:143]
	v_mfma_f32_16x16x32_bf16 v[136:139], v[92:95], v[164:167], v[136:139]
	v_mfma_f32_16x16x32_bf16 v[124:127], v[76:79], v[184:187], v[124:127]
	v_mfma_f32_16x16x32_bf16 v[120:123], v[92:95], v[184:187], v[120:123]
	v_mfma_f32_16x16x32_bf16 v[108:111], v[76:79], v[192:195], v[108:111]
	v_mfma_f32_16x16x32_bf16 v[104:107], v[92:95], v[192:195], v[104:107]
	v_mfma_f32_16x16x32_bf16 v[88:91], v[76:79], v[200:203], v[88:91]
	v_mfma_f32_16x16x32_bf16 v[80:83], v[92:95], v[200:203], v[80:83]
	s_setprio 0
	s_setprio 1
	v_mfma_f32_16x16x32_bf16 v[132:135], v[144:147], v[160:163], v[132:135]
	v_mfma_f32_16x16x32_bf16 v[128:131], v[152:155], v[160:163], v[128:131]
	v_mfma_f32_16x16x32_bf16 v[116:119], v[144:147], v[168:171], v[116:119]
	v_mfma_f32_16x16x32_bf16 v[112:115], v[152:155], v[168:171], v[112:115]
	v_mfma_f32_16x16x32_bf16 v[100:103], v[144:147], v[188:191], v[100:103]
	v_mfma_f32_16x16x32_bf16 v[96:99], v[152:155], v[188:191], v[96:99]
	v_mfma_f32_16x16x32_bf16 v[68:71], v[144:147], v[196:199], v[68:71]
	v_mfma_f32_16x16x32_bf16 v[64:67], v[152:155], v[196:199], v[64:67]
	v_mfma_f32_16x16x32_bf16 v[132:135], v[148:151], v[164:167], v[132:135]
	v_mfma_f32_16x16x32_bf16 v[128:131], v[156:159], v[164:167], v[128:131]
	v_mfma_f32_16x16x32_bf16 v[116:119], v[148:151], v[184:187], v[116:119]
	v_mfma_f32_16x16x32_bf16 v[112:115], v[156:159], v[184:187], v[112:115]
	v_mfma_f32_16x16x32_bf16 v[100:103], v[148:151], v[192:195], v[100:103]
	v_mfma_f32_16x16x32_bf16 v[96:99], v[156:159], v[192:195], v[96:99]
	v_mfma_f32_16x16x32_bf16 v[68:71], v[148:151], v[200:203], v[68:71]
	v_mfma_f32_16x16x32_bf16 v[64:67], v[156:159], v[200:203], v[64:67]
	s_barrier
	s_setprio 0
	ds_read_b128 v[160:163], v207 offset:16384
	ds_read_b128 v[164:167], v207 offset:17408
	ds_read_b128 v[168:171], v207 offset:18432
	ds_read_b128 v[184:187], v207 offset:19456
	ds_read_b128 v[188:191], v207 offset:20480
	ds_read_b128 v[192:195], v207 offset:21504
	ds_read_b128 v[196:199], v207 offset:22528
	ds_read_b128 v[200:203], v207 offset:23552
	s_mov_b32 m0, s31
	v_lshl_add_u64 v[204:205], s[48:49], 0, v[174:175]
	s_add_u32 s0, s48, 0x4000
	global_load_lds_dwordx4 v[204:205], off
	v_lshl_add_u64 v[204:205], s[48:49], 0, v[178:179]
	s_mov_b32 m0, s43
	s_addc_u32 s1, s49, 0
	global_load_lds_dwordx4 v[204:205], off
	v_lshl_add_u64 v[204:205], s[0:1], 0, v[174:175]
	s_mov_b32 m0, s53
	s_nop 0
	global_load_lds_dwordx4 v[204:205], off
	v_lshl_add_u64 v[204:205], s[0:1], 0, v[178:179]
	s_mov_b32 m0, s54
	s_nop 0
	global_load_lds_dwordx4 v[204:205], off
	v_lshl_add_u64 v[204:205], s[50:51], 0, v[172:173]
	s_mov_b32 m0, s56
	s_nop 0
	global_load_lds_dwordx4 v[204:205], off
	v_lshl_add_u64 v[204:205], s[50:51], 0, v[176:177]
	s_mov_b32 m0, s57
	s_nop 0
	global_load_lds_dwordx4 v[204:205], off
	s_waitcnt vmcnt(8)
	s_waitcnt lgkmcnt(0)
	s_setprio 1
	s_barrier
	v_mfma_f32_16x16x32_bf16 v[60:63], v[72:75], v[160:163], v[60:63]
	v_mfma_f32_16x16x32_bf16 v[56:59], v[84:87], v[160:163], v[56:59]
	v_mfma_f32_16x16x32_bf16 v[44:47], v[72:75], v[168:171], v[44:47]
	v_mfma_f32_16x16x32_bf16 v[40:43], v[84:87], v[168:171], v[40:43]
	v_mfma_f32_16x16x32_bf16 v[28:31], v[72:75], v[188:191], v[28:31]
	v_mfma_f32_16x16x32_bf16 v[24:27], v[84:87], v[188:191], v[24:27]
	v_mfma_f32_16x16x32_bf16 v[12:15], v[72:75], v[196:199], v[12:15]
	v_mfma_f32_16x16x32_bf16 v[8:11], v[84:87], v[196:199], v[8:11]
	v_mfma_f32_16x16x32_bf16 v[60:63], v[76:79], v[164:167], v[60:63]
	v_mfma_f32_16x16x32_bf16 v[56:59], v[92:95], v[164:167], v[56:59]
	v_mfma_f32_16x16x32_bf16 v[44:47], v[76:79], v[184:187], v[44:47]
	v_mfma_f32_16x16x32_bf16 v[40:43], v[92:95], v[184:187], v[40:43]
	v_mfma_f32_16x16x32_bf16 v[28:31], v[76:79], v[192:195], v[28:31]
	v_mfma_f32_16x16x32_bf16 v[24:27], v[92:95], v[192:195], v[24:27]
	v_mfma_f32_16x16x32_bf16 v[12:15], v[76:79], v[200:203], v[12:15]
	v_mfma_f32_16x16x32_bf16 v[8:11], v[92:95], v[200:203], v[8:11]
	s_setprio 0
	s_setprio 1
	v_mfma_f32_16x16x32_bf16 v[52:55], v[144:147], v[160:163], v[52:55]
	v_mfma_f32_16x16x32_bf16 v[48:51], v[152:155], v[160:163], v[48:51]
	v_mfma_f32_16x16x32_bf16 v[36:39], v[144:147], v[168:171], v[36:39]
	v_mfma_f32_16x16x32_bf16 v[32:35], v[152:155], v[168:171], v[32:35]
	v_mfma_f32_16x16x32_bf16 v[20:23], v[144:147], v[188:191], v[20:23]
	v_mfma_f32_16x16x32_bf16 v[16:19], v[152:155], v[188:191], v[16:19]
	v_mfma_f32_16x16x32_bf16 v[4:7], v[144:147], v[196:199], v[4:7]
	v_mfma_f32_16x16x32_bf16 v[0:3], v[152:155], v[196:199], v[0:3]
	v_mfma_f32_16x16x32_bf16 v[52:55], v[148:151], v[164:167], v[52:55]
	v_mfma_f32_16x16x32_bf16 v[48:51], v[156:159], v[164:167], v[48:51]
	v_mfma_f32_16x16x32_bf16 v[36:39], v[148:151], v[184:187], v[36:39]
	v_mfma_f32_16x16x32_bf16 v[32:35], v[156:159], v[184:187], v[32:35]
	v_mfma_f32_16x16x32_bf16 v[20:23], v[148:151], v[192:195], v[20:23]
	v_mfma_f32_16x16x32_bf16 v[16:19], v[156:159], v[192:195], v[16:19]
	v_mfma_f32_16x16x32_bf16 v[4:7], v[148:151], v[200:203], v[4:7]
	v_mfma_f32_16x16x32_bf16 v[0:3], v[156:159], v[200:203], v[0:3]
	s_barrier
	s_setprio 0
	v_add_u32_e32 v92, s64, v206
	v_add_u32_e32 v156, s69, v206
	ds_read_b128 v[72:75], v92
	ds_read_b128 v[76:79], v92 offset:1024
	ds_read_b128 v[84:87], v92 offset:2048
	ds_read_b128 v[92:95], v92 offset:3072
	ds_read_b128 v[144:147], v156
	ds_read_b128 v[148:151], v156 offset:1024
	ds_read_b128 v[152:155], v156 offset:2048
	ds_read_b128 v[156:159], v156 offset:3072
	ds_read_b128 v[160:163], v207 offset:32768
	ds_read_b128 v[164:167], v207 offset:33792
	ds_read_b128 v[168:171], v207 offset:34816
	ds_read_b128 v[184:187], v207 offset:35840
	ds_read_b128 v[188:191], v207 offset:36864
	ds_read_b128 v[192:195], v207 offset:37888
	ds_read_b128 v[196:199], v207 offset:38912
	ds_read_b128 v[200:203], v207 offset:39936
	s_add_u32 s0, s50, 0x4000
	s_addc_u32 s1, s51, 0
	s_mov_b32 m0, s58
	v_lshl_add_u64 v[204:205], s[0:1], 0, v[172:173]
	global_load_lds_dwordx4 v[204:205], off
	v_lshl_add_u64 v[204:205], s[0:1], 0, v[176:177]
	s_mov_b32 m0, s59
	s_nop 0
	global_load_lds_dwordx4 v[204:205], off
	s_waitcnt vmcnt(8)
	s_waitcnt lgkmcnt(0)
	s_setprio 1
	s_barrier
	v_mfma_f32_16x16x32_bf16 v[140:143], v[72:75], v[160:163], v[140:143]
	v_mfma_f32_16x16x32_bf16 v[136:139], v[84:87], v[160:163], v[136:139]
	v_mfma_f32_16x16x32_bf16 v[124:127], v[72:75], v[168:171], v[124:127]
	v_mfma_f32_16x16x32_bf16 v[120:123], v[84:87], v[168:171], v[120:123]
	v_mfma_f32_16x16x32_bf16 v[108:111], v[72:75], v[188:191], v[108:111]
	v_mfma_f32_16x16x32_bf16 v[104:107], v[84:87], v[188:191], v[104:107]
	v_mfma_f32_16x16x32_bf16 v[88:91], v[72:75], v[196:199], v[88:91]
	v_mfma_f32_16x16x32_bf16 v[80:83], v[84:87], v[196:199], v[80:83]
	v_mfma_f32_16x16x32_bf16 v[140:143], v[76:79], v[164:167], v[140:143]
	v_mfma_f32_16x16x32_bf16 v[136:139], v[92:95], v[164:167], v[136:139]
	v_mfma_f32_16x16x32_bf16 v[124:127], v[76:79], v[184:187], v[124:127]
	v_mfma_f32_16x16x32_bf16 v[120:123], v[92:95], v[184:187], v[120:123]
	v_mfma_f32_16x16x32_bf16 v[108:111], v[76:79], v[192:195], v[108:111]
	v_mfma_f32_16x16x32_bf16 v[104:107], v[92:95], v[192:195], v[104:107]
	v_mfma_f32_16x16x32_bf16 v[88:91], v[76:79], v[200:203], v[88:91]
	v_mfma_f32_16x16x32_bf16 v[80:83], v[92:95], v[200:203], v[80:83]
	s_setprio 0
	s_setprio 1
	v_mfma_f32_16x16x32_bf16 v[132:135], v[144:147], v[160:163], v[132:135]
	v_mfma_f32_16x16x32_bf16 v[128:131], v[152:155], v[160:163], v[128:131]
	v_mfma_f32_16x16x32_bf16 v[116:119], v[144:147], v[168:171], v[116:119]
	v_mfma_f32_16x16x32_bf16 v[112:115], v[152:155], v[168:171], v[112:115]
	v_mfma_f32_16x16x32_bf16 v[100:103], v[144:147], v[188:191], v[100:103]
	v_mfma_f32_16x16x32_bf16 v[96:99], v[152:155], v[188:191], v[96:99]
	v_mfma_f32_16x16x32_bf16 v[68:71], v[144:147], v[196:199], v[68:71]
	v_mfma_f32_16x16x32_bf16 v[64:67], v[152:155], v[196:199], v[64:67]
	v_mfma_f32_16x16x32_bf16 v[132:135], v[148:151], v[164:167], v[132:135]
	v_mfma_f32_16x16x32_bf16 v[128:131], v[156:159], v[164:167], v[128:131]
	v_mfma_f32_16x16x32_bf16 v[116:119], v[148:151], v[184:187], v[116:119]
	v_mfma_f32_16x16x32_bf16 v[112:115], v[156:159], v[184:187], v[112:115]
	v_mfma_f32_16x16x32_bf16 v[100:103], v[148:151], v[192:195], v[100:103]
	v_mfma_f32_16x16x32_bf16 v[96:99], v[156:159], v[192:195], v[96:99]
	v_mfma_f32_16x16x32_bf16 v[68:71], v[148:151], v[200:203], v[68:71]
	v_mfma_f32_16x16x32_bf16 v[64:67], v[156:159], v[200:203], v[64:67]
	s_barrier
	s_setprio 0
	ds_read_b128 v[160:163], v207 offset:49152
	ds_read_b128 v[164:167], v207 offset:50176
	ds_read_b128 v[168:171], v207 offset:51200
	ds_read_b128 v[184:187], v207 offset:52224
	ds_read_b128 v[188:191], v207 offset:53248
	ds_read_b128 v[192:195], v207 offset:54272
	ds_read_b128 v[196:199], v207 offset:55296
	ds_read_b128 v[200:203], v207 offset:56320
	s_add_u32 s0, s48, 0x8000
	s_addc_u32 s1, s49, 0
	s_mov_b32 m0, s65
	v_lshl_add_u64 v[204:205], s[0:1], 0, v[174:175]
	global_load_lds_dwordx4 v[204:205], off
	v_lshl_add_u64 v[204:205], s[0:1], 0, v[178:179]
	s_add_u32 s0, s48, 0xc000
	s_mov_b32 m0, s66
	s_addc_u32 s1, s49, 0
	global_load_lds_dwordx4 v[204:205], off
	v_lshl_add_u64 v[204:205], s[0:1], 0, v[174:175]
	s_mov_b32 m0, s70
	s_nop 0
	global_load_lds_dwordx4 v[204:205], off
	v_lshl_add_u64 v[204:205], s[0:1], 0, v[178:179]
	s_mov_b32 m0, s71
	s_nop 0
	global_load_lds_dwordx4 v[204:205], off
	v_lshl_add_u64 v[204:205], s[46:47], 0, v[172:173]
	s_mov_b32 m0, s67
	s_nop 0
	global_load_lds_dwordx4 v[204:205], off
	v_lshl_add_u64 v[204:205], s[46:47], 0, v[176:177]
	s_mov_b32 m0, s68
	s_nop 0
	global_load_lds_dwordx4 v[204:205], off
	s_waitcnt vmcnt(8)
	s_waitcnt lgkmcnt(0)
	s_setprio 1
	s_barrier
	v_mfma_f32_16x16x32_bf16 v[60:63], v[72:75], v[160:163], v[60:63]
	v_mfma_f32_16x16x32_bf16 v[56:59], v[84:87], v[160:163], v[56:59]
	v_mfma_f32_16x16x32_bf16 v[44:47], v[72:75], v[168:171], v[44:47]
	v_mfma_f32_16x16x32_bf16 v[40:43], v[84:87], v[168:171], v[40:43]
	v_mfma_f32_16x16x32_bf16 v[28:31], v[72:75], v[188:191], v[28:31]
	v_mfma_f32_16x16x32_bf16 v[24:27], v[84:87], v[188:191], v[24:27]
	v_mfma_f32_16x16x32_bf16 v[12:15], v[72:75], v[196:199], v[12:15]
	v_mfma_f32_16x16x32_bf16 v[8:11], v[84:87], v[196:199], v[8:11]
	v_mfma_f32_16x16x32_bf16 v[60:63], v[76:79], v[164:167], v[60:63]
	v_mfma_f32_16x16x32_bf16 v[56:59], v[92:95], v[164:167], v[56:59]
	v_mfma_f32_16x16x32_bf16 v[44:47], v[76:79], v[184:187], v[44:47]
	v_mfma_f32_16x16x32_bf16 v[40:43], v[92:95], v[184:187], v[40:43]
	v_mfma_f32_16x16x32_bf16 v[28:31], v[76:79], v[192:195], v[28:31]
	v_mfma_f32_16x16x32_bf16 v[24:27], v[92:95], v[192:195], v[24:27]
	v_mfma_f32_16x16x32_bf16 v[12:15], v[76:79], v[200:203], v[12:15]
	v_mfma_f32_16x16x32_bf16 v[8:11], v[92:95], v[200:203], v[8:11]
	s_setprio 0
	s_setprio 1
	v_mfma_f32_16x16x32_bf16 v[52:55], v[144:147], v[160:163], v[52:55]
	v_mfma_f32_16x16x32_bf16 v[48:51], v[152:155], v[160:163], v[48:51]
	v_mfma_f32_16x16x32_bf16 v[36:39], v[144:147], v[168:171], v[36:39]
	v_mfma_f32_16x16x32_bf16 v[32:35], v[152:155], v[168:171], v[32:35]
	v_mfma_f32_16x16x32_bf16 v[20:23], v[144:147], v[188:191], v[20:23]
	v_mfma_f32_16x16x32_bf16 v[16:19], v[152:155], v[188:191], v[16:19]
	v_mfma_f32_16x16x32_bf16 v[4:7], v[144:147], v[196:199], v[4:7]
	v_mfma_f32_16x16x32_bf16 v[0:3], v[152:155], v[196:199], v[0:3]
	v_mfma_f32_16x16x32_bf16 v[52:55], v[148:151], v[164:167], v[52:55]
	v_mfma_f32_16x16x32_bf16 v[48:51], v[156:159], v[164:167], v[48:51]
	v_mfma_f32_16x16x32_bf16 v[36:39], v[148:151], v[184:187], v[36:39]
	v_mfma_f32_16x16x32_bf16 v[32:35], v[156:159], v[184:187], v[32:35]
	v_mfma_f32_16x16x32_bf16 v[20:23], v[148:151], v[192:195], v[20:23]
	v_mfma_f32_16x16x32_bf16 v[16:19], v[156:159], v[192:195], v[16:19]
	v_mfma_f32_16x16x32_bf16 v[4:7], v[148:151], v[200:203], v[4:7]
	v_mfma_f32_16x16x32_bf16 v[0:3], v[156:159], v[200:203], v[0:3]
	s_barrier
	s_setprio 0
	s_add_i32 s76, s76, 2
	s_add_u32 s74, s74, 0x10000
	s_addc_u32 s75, s75, 0
	s_cmpk_gt_u32 s76, 0x7d
	s_mov_b64 s[0:1], s[44:45]
	s_cbranch_scc0 .LBB0_1248
	s_and_b64 vcc, exec, s[22:23]
	s_cbranch_vccz .LBB0_1251
	s_barrier
